# baseline (speedup 1.0000x reference)
.LBB3_45:
	v_add_u32_e32 v100, 0, v194
	s_nop 0
	ds_read_b128 v[96:99], v100
	ds_read_b128 v[100:103], v100 offset:2048
	s_waitcnt lgkmcnt(1)
	v_mfma_f32_16x16x32_f16 v[104:107], v[96:99], v[36:39], 0
	v_mfma_f32_16x16x32_f16 v[108:111], v[96:99], v[52:55], 0
	v_mfma_f32_16x16x32_f16 v[112:115], v[96:99], v[68:71], 0
	v_mfma_f32_16x16x32_f16 v[116:119], v[96:99], v[84:87], 0
	v_add_u32_e32 v96, 0, v195
	ds_read_b128 v[124:127], v96
	ds_read_b128 v[128:131], v96 offset:2048
	s_waitcnt lgkmcnt(1)
	v_add_u32_e32 v238, 0x12600, v137
	ds_read_b128 v[196:199], v238
	ds_read_b64 v[200:201], v238 offset:32
	ds_read_b128 v[202:205], v238 offset:16
	ds_read_b64 v[206:207], v238 offset:96
	ds_read_b128 v[208:211], v238 offset:80
	ds_read_b128 v[212:215], v238 offset:64
	ds_read_b64 v[216:217], v238 offset:544
	ds_read_b128 v[218:221], v238 offset:512
	ds_read_b128 v[222:225], v238 offset:528
	ds_read_b64 v[226:227], v238 offset:608
	ds_read_b128 v[228:231], v238 offset:592
	ds_read_b128 v[232:235], v238 offset:576
	v_mfma_f32_16x16x32_f16 v[120:123], v[124:127], v[44:47], v[104:107]
	v_mfma_f32_16x16x32_f16 v[108:111], v[124:127], v[60:63], v[108:111]
	v_mfma_f32_16x16x32_f16 v[96:99], v[124:127], v[76:79], v[112:115]
	v_mfma_f32_16x16x32_f16 v[142:145], v[124:127], v[92:95], v[116:119]
	v_mfma_f32_16x16x32_f16 v[104:107], v[100:103], v[36:39], 0
	v_mfma_f32_16x16x32_f16 v[112:115], v[100:103], v[52:55], 0
	v_mfma_f32_16x16x32_f16 v[124:127], v[100:103], v[68:71], 0
	v_mfma_f32_16x16x32_f16 v[132:135], v[100:103], v[84:87], 0
	s_waitcnt lgkmcnt(12)
	v_mfma_f32_16x16x32_f16 v[116:119], v[128:131], v[44:47], v[104:107]
	v_mfma_f32_16x16x32_f16 v[112:115], v[128:131], v[60:63], v[112:115]
	v_mfma_f32_16x16x32_f16 v[100:103], v[128:131], v[76:79], v[124:127]
	v_mfma_f32_16x16x32_f16 v[128:131], v[128:131], v[92:95], v[132:135]
	v_add_u32_e32 v140, 0, v137
	v_add_u32_e32 v104, 0x12600, v140
	s_nop 0
	v_add_u32_e32 v124, 0x12620, v140
	s_nop 0
	v_add_u32_e32 v124, 0x12610, v140
	s_nop 0
	s_waitcnt lgkmcnt(0)
	v_add_u32_e32 v239, s0, v189
	v_xor_b32_e32 v239, v239, v188
	v_lshl_add_u32 v239, v239, 4, v190
	ds_read_b128 v[240:243], v239 offset:32768
	ds_read_b128 v[244:247], v239 offset:36864
	ds_read_b128 v[248:251], v239 offset:40960
	ds_read_b128 v[252:255], v239 offset:45056
	v_fma_f32 v132, v196, v120, v108
	v_fma_f32 v132, -v197, v121, v132
	v_fma_f32 v133, v196, v121, v109
	v_fmac_f32_e32 v133, v197, v120
	v_fma_f32 v134, v196, v132, v96
	v_fma_f32 v134, -v197, v133, v134
	v_fma_f32 v133, v196, v133, v97
	v_fmac_f32_e32 v133, v197, v132
	v_fma_f32 v132, v196, v134, v142
	v_fma_f32 v132, -v197, v133, v132
	v_fma_f32 v143, v196, v133, v143
	v_fmac_f32_e32 v143, v197, v134
	v_mov_b32_dpp v133, v132 row_shr:1 row_mask:0xf bank_mask:0xf bound_ctrl:1
	v_fmac_f32_e32 v132, v198, v133
	v_mov_b32_dpp v134, v143 row_shr:1 row_mask:0xf bank_mask:0xf bound_ctrl:1
	v_fma_f32 v132, -v199, v134, v132
	v_fmac_f32_e32 v143, v198, v134
	v_fmac_f32_e32 v143, v199, v133
	v_mov_b32_dpp v106, v132 row_shr:2 row_mask:0xf bank_mask:0xf bound_ctrl:1
	v_add_u32_e32 v133, 0x12660, v140
	v_mov_b32_dpp v107, v143 row_shr:2 row_mask:0xf bank_mask:0xf bound_ctrl:1
	s_nop 0
	s_nop 0
	v_fmac_f32_e32 v132, v202, v106
	v_fma_f32 v132, -v203, v107, v132
	v_fmac_f32_e32 v143, v202, v107
	v_fmac_f32_e32 v143, v203, v106
	v_mov_b32_dpp v106, v132 row_shr:4 row_mask:0xf bank_mask:0xf bound_ctrl:1
	v_fmac_f32_e32 v132, v204, v106
	v_mov_b32_dpp v107, v143 row_shr:4 row_mask:0xf bank_mask:0xf bound_ctrl:1
	v_fma_f32 v124, -v205, v107, v132
	v_fmac_f32_e32 v143, v204, v107
	v_fmac_f32_e32 v143, v205, v106
	v_mov_b32_dpp v106, v124 row_shr:8 row_mask:0xf bank_mask:0xf bound_ctrl:1
	v_fmac_f32_e32 v124, v200, v106
	v_mov_b32_dpp v107, v143 row_shr:8 row_mask:0xf bank_mask:0xf bound_ctrl:1
	v_fma_f32 v142, -v201, v107, v124
	v_add_u32_e32 v124, 0x12640, v140
	v_add_u32_e32 v125, 0x12650, v140
	s_nop 0
	s_nop 0
	v_fmac_f32_e32 v143, v200, v107
	v_fmac_f32_e32 v143, v201, v106
	v_xor_b32_e32 v141, 0x80000000, v197
	v_mov_b32_dpp v142, v142 row_shr:1 row_mask:0xf bank_mask:0xf bound_ctrl:1
	s_nop 0
	v_fma_f32 v106, v212, v122, v110
	v_fma_f32 v106, -v213, v123, v106
	v_fma_f32 v146, v212, v123, v111
	v_fmac_f32_e32 v146, v213, v122
	v_fma_f32 v147, v212, v106, v98
	v_fma_f32 v147, -v213, v146, v147
	v_fma_f32 v146, v212, v146, v99
	v_fmac_f32_e32 v146, v213, v106
	v_fma_f32 v106, v212, v147, v144
	v_fma_f32 v106, -v213, v146, v106
	v_fmac_f32_e32 v145, v212, v146
	v_fmac_f32_e32 v145, v213, v147
	v_mov_b32_dpp v144, v106 row_shr:1 row_mask:0xf bank_mask:0xf bound_ctrl:1
	v_fmac_f32_e32 v106, v214, v144
	v_mov_b32_dpp v146, v145 row_shr:1 row_mask:0xf bank_mask:0xf bound_ctrl:1
	v_fma_f32 v106, -v215, v146, v106
	v_fmac_f32_e32 v145, v214, v146
	v_fmac_f32_e32 v145, v215, v144
	v_mov_b32_dpp v126, v106 row_shr:2 row_mask:0xf bank_mask:0xf bound_ctrl:1
	v_fmac_f32_e32 v106, v208, v126
	v_mov_b32_dpp v127, v145 row_shr:2 row_mask:0xf bank_mask:0xf bound_ctrl:1
	v_fma_f32 v106, -v209, v127, v106
	v_fmac_f32_e32 v145, v208, v127
	v_fmac_f32_e32 v145, v209, v126
	v_mov_b32_dpp v126, v106 row_shr:4 row_mask:0xf bank_mask:0xf bound_ctrl:1
	v_fmac_f32_e32 v106, v210, v126
	v_mov_b32_dpp v127, v145 row_shr:4 row_mask:0xf bank_mask:0xf bound_ctrl:1
	v_fma_f32 v106, -v211, v127, v106
	v_fmac_f32_e32 v145, v210, v127
	v_fmac_f32_e32 v145, v211, v126
	v_mov_b32_dpp v126, v106 row_shr:8 row_mask:0xf bank_mask:0xf bound_ctrl:1
	v_fmac_f32_e32 v106, v206, v126
	v_mov_b32_dpp v127, v145 row_shr:8 row_mask:0xf bank_mask:0xf bound_ctrl:1
	v_fma_f32 v106, -v207, v127, v106
	v_fmac_f32_e32 v145, v206, v127
	v_add_u32_e32 v127, 0x12820, v140
	v_fmac_f32_e32 v145, v207, v126
	v_add_u32_e32 v126, 0x12800, v140
	s_nop 0
	s_nop 0
	v_mov_b32_dpp v150, v106 row_shr:1 row_mask:0xf bank_mask:0xf bound_ctrl:1
	v_add_u32_e32 v106, 0x12810, v140
	v_mov_b32_dpp v151, v145 row_shr:1 row_mask:0xf bank_mask:0xf bound_ctrl:1
	s_nop 0
	s_nop 0
	v_fma_f32 v106, v218, v116, v112
	v_fma_f32 v106, -v219, v117, v106
	v_fma_f32 v126, v218, v117, v113
	v_fmac_f32_e32 v126, v219, v116
	v_fma_f32 v127, v218, v106, v100
	v_fma_f32 v127, -v219, v126, v127
	v_fma_f32 v126, v218, v126, v101
	v_fmac_f32_e32 v126, v219, v106
	v_fma_f32 v152, v218, v126, v129
	v_fma_f32 v106, v218, v127, v128
	v_fmac_f32_e32 v152, v219, v127
	v_fma_f32 v106, -v219, v126, v106
	v_add_u32_e32 v128, 0x12860, v140
	v_mov_b32_dpp v127, v152 row_shr:1 row_mask:0xf bank_mask:0xf bound_ctrl:1
	v_mov_b32_dpp v126, v106 row_shr:1 row_mask:0xf bank_mask:0xf bound_ctrl:1
	v_fmac_f32_e32 v152, v220, v127
	v_fmac_f32_e32 v106, v220, v126
	v_fmac_f32_e32 v152, v221, v126
	v_fma_f32 v106, -v221, v127, v106
	s_nop 0
	v_mov_b32_dpp v127, v152 row_shr:2 row_mask:0xf bank_mask:0xf bound_ctrl:1
	v_mov_b32_dpp v126, v106 row_shr:2 row_mask:0xf bank_mask:0xf bound_ctrl:1
	s_nop 0
	v_fmac_f32_e32 v152, v222, v127
	v_fmac_f32_e32 v106, v222, v126
	v_fmac_f32_e32 v152, v223, v126
	v_fma_f32 v106, -v223, v127, v106
	v_add_u32_e32 v144, 0x12840, v140
	v_mov_b32_dpp v127, v152 row_shr:4 row_mask:0xf bank_mask:0xf bound_ctrl:1
	v_mov_b32_dpp v126, v106 row_shr:4 row_mask:0xf bank_mask:0xf bound_ctrl:1
	v_fmac_f32_e32 v152, v224, v127
	v_fmac_f32_e32 v106, v224, v126
	v_fmac_f32_e32 v152, v225, v126
	v_add_u32_e32 v126, 0x12850, v140
	v_fma_f32 v106, -v225, v127, v106
	s_nop 0
	s_nop 0
	v_mov_b32_dpp v154, v106 row_shr:8 row_mask:0xf bank_mask:0xf bound_ctrl:1
	v_mov_b32_dpp v155, v152 row_shr:8 row_mask:0xf bank_mask:0xf bound_ctrl:1
	v_fmac_f32_e32 v106, v216, v154
	v_fma_f32 v106, -v217, v155, v106
	v_fmac_f32_e32 v152, v216, v155
	v_fmac_f32_e32 v152, v217, v154
	v_mov_b32_dpp v148, v106 row_shr:1 row_mask:0xf bank_mask:0xf bound_ctrl:1
	s_nop 0
	v_fma_f32 v106, v232, v118, v114
	v_fma_f32 v106, -v233, v119, v106
	v_fma_f32 v140, v232, v119, v115
	v_mov_b32_dpp v149, v152 row_shr:1 row_mask:0xf bank_mask:0xf bound_ctrl:1
	v_fmac_f32_e32 v140, v233, v118
	v_fma_f32 v152, v232, v106, v102
	v_fma_f32 v152, -v233, v140, v152
	v_fma_f32 v140, v232, v140, v103
	v_fmac_f32_e32 v140, v233, v106
	v_fma_f32 v106, v232, v152, v130
	v_fmac_f32_e32 v131, v232, v140
	v_fma_f32 v106, -v233, v140, v106
	v_fmac_f32_e32 v131, v233, v152
	v_mov_b32_dpp v143, v143 row_shr:1 row_mask:0xf bank_mask:0xf bound_ctrl:1
	v_mov_b32_dpp v130, v106 row_shr:1 row_mask:0xf bank_mask:0xf bound_ctrl:1
	v_mov_b32_dpp v140, v131 row_shr:1 row_mask:0xf bank_mask:0xf bound_ctrl:1
	v_fmac_f32_e32 v106, v234, v130
	v_fmac_f32_e32 v131, v234, v140
	v_fma_f32 v106, -v235, v140, v106
	v_fmac_f32_e32 v131, v235, v130
	v_xor_b32_e32 v107, 0x80000000, v213
	v_mov_b32_dpp v130, v106 row_shr:2 row_mask:0xf bank_mask:0xf bound_ctrl:1
	v_mov_b32_dpp v140, v131 row_shr:2 row_mask:0xf bank_mask:0xf bound_ctrl:1
	v_fmac_f32_e32 v106, v228, v130
	v_fmac_f32_e32 v131, v228, v140
	v_fma_f32 v106, -v229, v140, v106
	v_fmac_f32_e32 v131, v229, v130
	v_xor_b32_e32 v153, 0x80000000, v219
	v_mov_b32_dpp v126, v106 row_shr:4 row_mask:0xf bank_mask:0xf bound_ctrl:1
	v_mov_b32_dpp v127, v131 row_shr:4 row_mask:0xf bank_mask:0xf bound_ctrl:1
	v_fmac_f32_e32 v106, v230, v126
	v_fmac_f32_e32 v131, v230, v127
	v_fma_f32 v106, -v231, v127, v106
	v_fmac_f32_e32 v131, v231, v126
	v_xor_b32_e32 v155, 0x80000000, v233
	v_mov_b32_dpp v126, v106 row_shr:8 row_mask:0xf bank_mask:0xf bound_ctrl:1
	v_mov_b32_dpp v127, v131 row_shr:8 row_mask:0xf bank_mask:0xf bound_ctrl:1
	v_fmac_f32_e32 v106, v226, v126
	v_fmac_f32_e32 v131, v226, v127
	v_fma_f32 v106, -v227, v127, v106
	v_fmac_f32_e32 v131, v227, v126
	s_nop 0
	v_mov_b32_dpp v126, v106 row_shr:1 row_mask:0xf bank_mask:0xf bound_ctrl:1
	v_mov_b32_dpp v127, v131 row_shr:1 row_mask:0xf bank_mask:0xf bound_ctrl:1
	v_pk_fma_f32 v[120:121], v[196:197], v[142:143], v[120:121] op_sel_hi:[0,1,1]
	v_pk_fma_f32 v[128:129], v[218:219], v[148:149], v[116:117] op_sel_hi:[0,1,1]
	v_pk_fma_f32 v[122:123], v[212:213], v[150:151], v[122:123] op_sel_hi:[0,1,1]
	v_pk_fma_f32 v[130:131], v[232:233], v[126:127], v[118:119] op_sel_hi:[0,1,1]
	v_cvt_pk_f16_f32 v119, v126, v127
	v_add_u32_e32 v134, s0, v189
	v_pk_fma_f32 v[120:121], v[196:197], v[142:143], v[120:121] op_sel:[1,0,1] op_sel_hi:[1,1,0] neg_hi:[1,0,0]
	v_pk_fma_f32 v[128:129], v[218:219], v[148:149], v[128:129] op_sel:[1,0,1] op_sel_hi:[1,1,0] neg_hi:[1,0,0]
	v_pk_fma_f32 v[122:123], v[212:213], v[150:151], v[122:123] op_sel:[1,0,1] op_sel_hi:[1,1,0] neg_hi:[1,0,0]
	v_pk_fma_f32 v[126:127], v[232:233], v[126:127], v[130:131] op_sel:[1,0,1] op_sel_hi:[1,1,0] neg_hi:[1,0,0]
	v_mov_b32_e32 v140, v197
	v_mov_b32_e32 v152, v219
	v_mov_b32_e32 v106, v213
	v_mov_b32_e32 v154, v233
	v_cvt_pk_f16_f32 v116, v142, v143
	v_xor_b32_e32 v142, v134, v188
	v_pk_fma_f32 v[130:131], v[196:197], v[120:121], v[108:109] op_sel:[0,1,0] op_sel_hi:[0,0,1]
	v_pk_fma_f32 v[112:113], v[218:219], v[128:129], v[112:113] op_sel:[0,1,0] op_sel_hi:[0,0,1]
	v_pk_fma_f32 v[134:135], v[212:213], v[122:123], v[110:111] op_sel:[0,1,0] op_sel_hi:[0,0,1]
	v_pk_fma_f32 v[114:115], v[232:233], v[126:127], v[114:115] op_sel:[0,1,0] op_sel_hi:[0,0,1]
	v_cvt_pk_f16_f32 v111, v127, v126
	v_cvt_pk_f16_f32 v110, v129, v128
	v_lshl_add_u32 v142, v142, 4, v190
	v_pk_fma_f32 v[130:131], v[140:141], v[120:121], v[130:131] op_sel:[1,0,0] op_sel_hi:[0,1,1]
	v_pk_fma_f32 v[128:129], v[152:153], v[128:129], v[112:113] op_sel:[1,0,0] op_sel_hi:[0,1,1]
	v_pk_fma_f32 v[106:107], v[106:107], v[122:123], v[134:135] op_sel:[1,0,0] op_sel_hi:[0,1,1]
	v_pk_fma_f32 v[126:127], v[154:155], v[126:127], v[114:115] op_sel:[1,0,0] op_sel_hi:[0,1,1]
	v_cvt_pk_f16_f32 v109, v123, v122
	v_cvt_pk_f16_f32 v108, v121, v120
	s_nop 0
	s_nop 0
	v_pk_fma_f32 v[134:135], v[196:197], v[130:131], v[96:97] op_sel_hi:[0,1,1]
	v_pk_fma_f32 v[100:101], v[218:219], v[128:129], v[100:101] op_sel_hi:[0,1,1]
	v_pk_fma_f32 v[140:141], v[212:213], v[106:107], v[98:99] op_sel_hi:[0,1,1]
	v_pk_fma_f32 v[102:103], v[232:233], v[126:127], v[102:103] op_sel_hi:[0,1,1]
	v_cvt_pk_f16_f32 v97, v106, v107
	v_pk_fma_f32 v[104:105], v[196:197], v[130:131], v[134:135] op_sel:[1,0,1] op_sel_hi:[1,1,0] neg_hi:[1,0,0]
	v_pk_fma_f32 v[100:101], v[218:219], v[128:129], v[100:101] op_sel:[1,0,1] op_sel_hi:[1,1,0] neg_hi:[1,0,0]
	v_pk_fma_f32 v[106:107], v[212:213], v[106:107], v[140:141] op_sel:[1,0,1] op_sel_hi:[1,1,0] neg_hi:[1,0,0]
	v_pk_fma_f32 v[102:103], v[232:233], v[126:127], v[102:103] op_sel:[1,0,1] op_sel_hi:[1,1,0] neg_hi:[1,0,0]
	v_cvt_pk_f16_f32 v104, v104, v105
	v_cvt_pk_f16_f32 v105, v100, v101
	v_cvt_pk_f16_f32 v100, v106, v107
	v_cvt_pk_f16_f32 v103, v102, v103
	v_cvt_pk_f16_f32 v118, v148, v149
	v_cvt_pk_f16_f32 v117, v150, v151
	v_cvt_pk_f16_f32 v99, v126, v127
	v_cvt_pk_f16_f32 v98, v128, v129
	v_cvt_pk_f16_f32 v96, v130, v131
	v_alignbit_b32 v101, v100, v100, 16
	v_alignbit_b32 v100, v104, v104, 16
	v_alignbit_b32 v102, v105, v105, 16
	v_alignbit_b32 v103, v103, v103, 16
	s_nop 0
	v_mfma_f32_16x16x32_f16 v[88:91], v[240:243], v[116:119], v[88:91]
	s_add_i32 s0, s0, 4
	v_add_u32_e32 v137, 0x400, v137
	v_add_u32_e32 v194, 0x1000, v194
	v_mfma_f32_16x16x32_f16 v[80:83], v[240:243], v[108:111], v[80:83]
	s_cmp_lg_u32 s0, 16
	v_add_u32_e32 v195, 0x1000, v195
	v_mfma_f32_16x16x32_f16 v[72:75], v[240:243], v[96:99], v[72:75]
	v_mfma_f32_16x16x32_f16 v[64:67], v[240:243], v[100:103], v[64:67]
	s_nop 0
	s_nop 0
	s_waitcnt lgkmcnt(2)
	v_mfma_f32_16x16x32_f16 v[56:59], v[244:247], v[116:119], v[56:59]
	v_mfma_f32_16x16x32_f16 v[48:51], v[244:247], v[108:111], v[48:51]
	v_mfma_f32_16x16x32_f16 v[40:43], v[244:247], v[96:99], v[40:43]
	v_mfma_f32_16x16x32_f16 v[32:35], v[244:247], v[100:103], v[32:35]
	s_waitcnt lgkmcnt(1)
	v_mfma_f32_16x16x32_f16 v[28:31], v[248:251], v[116:119], v[28:31]
	v_mfma_f32_16x16x32_f16 v[24:27], v[248:251], v[108:111], v[24:27]
	v_mfma_f32_16x16x32_f16 v[20:23], v[248:251], v[96:99], v[20:23]
	v_mfma_f32_16x16x32_f16 v[16:19], v[248:251], v[100:103], v[16:19]
	s_waitcnt lgkmcnt(0)
	v_mfma_f32_16x16x32_f16 v[12:15], v[252:255], v[116:119], v[12:15]
	v_mfma_f32_16x16x32_f16 v[8:11], v[252:255], v[108:111], v[8:11]
	v_mfma_f32_16x16x32_f16 v[4:7], v[252:255], v[96:99], v[4:7]
	v_mfma_f32_16x16x32_f16 v[0:3], v[252:255], v[100:103], v[0:3]
	s_cbranch_scc1 .LBB3_45
	s_mov_b32 s0, 0
.LBB3_47:
	v_add_u32_e32 v100, 0, v175
	ds_read_b128 v[96:99], v100
	ds_read_b128 v[100:103], v100 offset:2048
	s_waitcnt lgkmcnt(1)
	v_mfma_f32_16x16x32_f16 v[104:107], v[96:99], v[36:39], 0
	v_mfma_f32_16x16x32_f16 v[108:111], v[96:99], v[52:55], 0
	v_mfma_f32_16x16x32_f16 v[112:115], v[96:99], v[68:71], 0
	v_mfma_f32_16x16x32_f16 v[116:119], v[96:99], v[84:87], 0
	v_add_u32_e32 v96, 0, v174
	ds_read_b128 v[120:123], v96
	ds_read_b128 v[124:127], v96 offset:2048
	s_waitcnt lgkmcnt(1)
	v_add_u32_e32 v238, 0x12600, v179
	ds_read_b128 v[196:199], v238
	ds_read_b64 v[200:201], v238 offset:32
	ds_read_b128 v[202:205], v238 offset:16
	ds_read_b64 v[206:207], v238 offset:96
	ds_read_b128 v[208:211], v238 offset:80
	ds_read_b128 v[212:215], v238 offset:64
	ds_read_b64 v[216:217], v238 offset:544
	ds_read_b128 v[218:221], v238 offset:512
	ds_read_b128 v[222:225], v238 offset:528
	ds_read_b64 v[226:227], v238 offset:608
	ds_read_b128 v[228:231], v238 offset:592
	ds_read_b128 v[232:235], v238 offset:576
	v_mfma_f32_16x16x32_f16 v[132:135], v[120:123], v[44:47], v[104:107]
	v_mfma_f32_16x16x32_f16 v[96:99], v[120:123], v[60:63], v[108:111]
	v_mfma_f32_16x16x32_f16 v[104:107], v[120:123], v[76:79], v[112:115]
	v_mfma_f32_16x16x32_f16 v[120:123], v[120:123], v[92:95], v[116:119]
	v_mfma_f32_16x16x32_f16 v[108:111], v[100:103], v[36:39], 0
	v_mfma_f32_16x16x32_f16 v[112:115], v[100:103], v[52:55], 0
	v_mfma_f32_16x16x32_f16 v[116:119], v[100:103], v[68:71], 0
	v_mfma_f32_16x16x32_f16 v[140:143], v[100:103], v[84:87], 0
	s_waitcnt lgkmcnt(12)
	v_mfma_f32_16x16x32_f16 v[128:131], v[124:127], v[44:47], v[108:111]
	v_mfma_f32_16x16x32_f16 v[100:103], v[124:127], v[60:63], v[112:115]
	v_mfma_f32_16x16x32_f16 v[112:115], v[124:127], v[76:79], v[116:119]
	v_mfma_f32_16x16x32_f16 v[116:119], v[124:127], v[92:95], v[140:143]
	v_add_u32_e32 v137, 0, v179
	v_add_u32_e32 v108, 0x12600, v137
	s_nop 0
	v_add_u32_e32 v124, 0x12620, v137
	s_nop 0
	v_add_u32_e32 v124, 0x12610, v137
	s_nop 0
	s_waitcnt lgkmcnt(0)
	v_add_u32_e32 v239, s0, v189
	v_xor_b32_e32 v239, v239, v188
	v_lshl_add_u32 v239, v239, 4, v190
	ds_read_b128 v[240:243], v239 offset:49152
	ds_read_b128 v[244:247], v239 offset:53248
	ds_read_b128 v[248:251], v239 offset:57344
	ds_read_b128 v[252:255], v239 offset:61440
	v_fma_f32 v140, v196, v120, v104
	v_fma_f32 v140, -v197, v121, v140
	v_fma_f32 v141, v196, v121, v105
	v_fmac_f32_e32 v141, v197, v120
	v_fma_f32 v142, v196, v140, v96
	v_fma_f32 v142, -v197, v141, v142
	v_fma_f32 v141, v196, v141, v97
	v_fmac_f32_e32 v141, v197, v140
	v_fma_f32 v132, v196, v142, v132
	v_fma_f32 v132, -v197, v141, v132
	v_fma_f32 v146, v196, v141, v133
	v_fmac_f32_e32 v146, v197, v142
	v_mov_b32_dpp v133, v132 row_shl:1 row_mask:0xf bank_mask:0xf bound_ctrl:1
	v_fmac_f32_e32 v132, v198, v133
	v_mov_b32_dpp v140, v146 row_shl:1 row_mask:0xf bank_mask:0xf bound_ctrl:1
	v_fma_f32 v141, -v199, v140, v132
	v_fmac_f32_e32 v146, v198, v140
	v_fmac_f32_e32 v146, v199, v133
	v_mov_b32_dpp v110, v141 row_shl:2 row_mask:0xf bank_mask:0xf bound_ctrl:1
	v_add_u32_e32 v132, 0x12660, v137
	v_mov_b32_dpp v111, v146 row_shl:2 row_mask:0xf bank_mask:0xf bound_ctrl:1
	s_nop 0
	s_nop 0
	v_fmac_f32_e32 v141, v202, v110
	v_fma_f32 v140, -v203, v111, v141
	v_fmac_f32_e32 v146, v202, v111
	v_fmac_f32_e32 v146, v203, v110
	v_mov_b32_dpp v110, v140 row_shl:4 row_mask:0xf bank_mask:0xf bound_ctrl:1
	v_fmac_f32_e32 v140, v204, v110
	v_mov_b32_dpp v111, v146 row_shl:4 row_mask:0xf bank_mask:0xf bound_ctrl:1
	v_fma_f32 v124, -v205, v111, v140
	v_fmac_f32_e32 v146, v204, v111
	v_fmac_f32_e32 v146, v205, v110
	v_mov_b32_dpp v110, v124 row_shl:8 row_mask:0xf bank_mask:0xf bound_ctrl:1
	v_fmac_f32_e32 v124, v200, v110
	v_mov_b32_dpp v111, v146 row_shl:8 row_mask:0xf bank_mask:0xf bound_ctrl:1
	v_fma_f32 v147, -v201, v111, v124
	v_add_u32_e32 v124, 0x12640, v137
	v_add_u32_e32 v125, 0x12650, v137
	s_nop 0
	s_nop 0
	v_fmac_f32_e32 v146, v200, v111
	v_fmac_f32_e32 v146, v201, v110
	v_mov_b32_dpp v110, v147 row_shl:1 row_mask:0xf bank_mask:0xf bound_ctrl:1
	s_nop 0
	v_fma_f32 v144, v212, v122, v106
	v_fma_f32 v144, -v213, v123, v144
	v_fma_f32 v145, v212, v123, v107
	v_mov_b32_dpp v111, v146 row_shl:1 row_mask:0xf bank_mask:0xf bound_ctrl:1
	v_fmac_f32_e32 v145, v213, v122
	v_fma_f32 v146, v212, v144, v98
	v_fma_f32 v146, -v213, v145, v146
	v_fma_f32 v145, v212, v145, v99
	v_fmac_f32_e32 v145, v213, v144
	v_fma_f32 v134, v212, v146, v134
	v_fma_f32 v134, -v213, v145, v134
	v_fmac_f32_e32 v135, v212, v145
	v_fmac_f32_e32 v135, v213, v146
	v_mov_b32_dpp v144, v134 row_shl:1 row_mask:0xf bank_mask:0xf bound_ctrl:1
	v_fmac_f32_e32 v134, v214, v144
	v_mov_b32_dpp v145, v135 row_shl:1 row_mask:0xf bank_mask:0xf bound_ctrl:1
	v_fma_f32 v134, -v215, v145, v134
	v_fmac_f32_e32 v135, v214, v145
	v_fmac_f32_e32 v135, v215, v144
	v_mov_b32_dpp v126, v134 row_shl:2 row_mask:0xf bank_mask:0xf bound_ctrl:1
	v_fmac_f32_e32 v134, v208, v126
	v_mov_b32_dpp v127, v135 row_shl:2 row_mask:0xf bank_mask:0xf bound_ctrl:1
	v_fma_f32 v134, -v209, v127, v134
	v_fmac_f32_e32 v135, v208, v127
	v_fmac_f32_e32 v135, v209, v126
	v_mov_b32_dpp v126, v134 row_shl:4 row_mask:0xf bank_mask:0xf bound_ctrl:1
	v_fmac_f32_e32 v134, v210, v126
	v_mov_b32_dpp v127, v135 row_shl:4 row_mask:0xf bank_mask:0xf bound_ctrl:1
	v_fma_f32 v134, -v211, v127, v134
	v_fmac_f32_e32 v135, v210, v127
	v_fmac_f32_e32 v135, v211, v126
	v_mov_b32_dpp v126, v134 row_shl:8 row_mask:0xf bank_mask:0xf bound_ctrl:1
	v_fmac_f32_e32 v134, v206, v126
	v_mov_b32_dpp v127, v135 row_shl:8 row_mask:0xf bank_mask:0xf bound_ctrl:1
	v_fma_f32 v134, -v207, v127, v134
	v_fmac_f32_e32 v135, v206, v127
	v_add_u32_e32 v127, 0x12820, v137
	v_fmac_f32_e32 v135, v207, v126
	v_add_u32_e32 v126, 0x12800, v137
	s_nop 0
	s_nop 0
	v_add_u32_e32 v132, 0x12810, v137
	v_mov_b32_dpp v126, v134 row_shl:1 row_mask:0xf bank_mask:0xf bound_ctrl:1
	v_mov_b32_dpp v127, v135 row_shl:1 row_mask:0xf bank_mask:0xf bound_ctrl:1
	s_nop 0
	s_nop 0
	v_fma_f32 v144, v218, v116, v112
	v_fma_f32 v144, -v219, v117, v144
	v_fma_f32 v145, v218, v117, v113
	v_fmac_f32_e32 v145, v219, v116
	v_fma_f32 v148, v218, v144, v100
	v_fma_f32 v148, -v219, v145, v148
	v_fma_f32 v145, v218, v145, v101
	v_fmac_f32_e32 v145, v219, v144
	v_fma_f32 v128, v218, v148, v128
	v_fma_f32 v128, -v219, v145, v128
	v_fma_f32 v149, v218, v145, v129
	v_fmac_f32_e32 v149, v219, v148
	v_mov_b32_dpp v129, v128 row_shl:1 row_mask:0xf bank_mask:0xf bound_ctrl:1
	v_fmac_f32_e32 v128, v220, v129
	v_mov_b32_dpp v144, v149 row_shl:1 row_mask:0xf bank_mask:0xf bound_ctrl:1
	v_fma_f32 v145, -v221, v144, v128
	v_fmac_f32_e32 v149, v220, v144
	v_fmac_f32_e32 v149, v221, v129
	v_mov_b32_dpp v142, v145 row_shl:2 row_mask:0xf bank_mask:0xf bound_ctrl:1
	v_add_u32_e32 v128, 0x12860, v137
	v_mov_b32_dpp v143, v149 row_shl:2 row_mask:0xf bank_mask:0xf bound_ctrl:1
	s_nop 0
	s_nop 0
	v_fmac_f32_e32 v145, v222, v142
	v_fma_f32 v144, -v223, v143, v145
	v_fmac_f32_e32 v149, v222, v143
	v_fmac_f32_e32 v149, v223, v142
	v_mov_b32_dpp v132, v144 row_shl:4 row_mask:0xf bank_mask:0xf bound_ctrl:1
	v_fmac_f32_e32 v144, v224, v132
	v_mov_b32_dpp v133, v149 row_shl:4 row_mask:0xf bank_mask:0xf bound_ctrl:1
	v_fma_f32 v142, -v225, v133, v144
	v_fmac_f32_e32 v149, v224, v133
	v_fmac_f32_e32 v149, v225, v132
	v_mov_b32_dpp v148, v142 row_shl:8 row_mask:0xf bank_mask:0xf bound_ctrl:1
	v_fmac_f32_e32 v142, v216, v148
	v_mov_b32_dpp v150, v149 row_shl:8 row_mask:0xf bank_mask:0xf bound_ctrl:1
	v_fma_f32 v151, -v217, v150, v142
	v_add_u32_e32 v142, 0x12840, v137
	v_add_u32_e32 v132, 0x12850, v137
	s_nop 0
	s_nop 0
	v_fmac_f32_e32 v149, v216, v150
	v_fmac_f32_e32 v149, v217, v148
	v_mov_b32_dpp v146, v151 row_shl:1 row_mask:0xf bank_mask:0xf bound_ctrl:1
	s_nop 0
	v_fma_f32 v137, v232, v118, v114
	v_fma_f32 v137, -v233, v119, v137
	v_fma_f32 v148, v232, v119, v115
	v_mov_b32_dpp v147, v149 row_shl:1 row_mask:0xf bank_mask:0xf bound_ctrl:1
	v_fmac_f32_e32 v148, v233, v118
	v_fma_f32 v149, v232, v137, v102
	v_fma_f32 v149, -v233, v148, v149
	v_fma_f32 v148, v232, v148, v103
	v_fmac_f32_e32 v148, v233, v137
	v_fma_f32 v130, v232, v149, v130
	v_fmac_f32_e32 v131, v232, v148
	v_fma_f32 v130, -v233, v148, v130
	v_fmac_f32_e32 v131, v233, v149
	s_nop 0
	v_mov_b32_dpp v137, v130 row_shl:1 row_mask:0xf bank_mask:0xf bound_ctrl:1
	v_mov_b32_dpp v148, v131 row_shl:1 row_mask:0xf bank_mask:0xf bound_ctrl:1
	v_fmac_f32_e32 v130, v234, v137
	v_fmac_f32_e32 v131, v234, v148
	v_fma_f32 v130, -v235, v148, v130
	v_fmac_f32_e32 v131, v235, v137
	s_nop 0
	v_mov_b32_dpp v137, v130 row_shl:2 row_mask:0xf bank_mask:0xf bound_ctrl:1
	v_mov_b32_dpp v144, v131 row_shl:2 row_mask:0xf bank_mask:0xf bound_ctrl:1
	v_fmac_f32_e32 v130, v228, v137
	v_fmac_f32_e32 v131, v228, v144
	v_fma_f32 v130, -v229, v144, v130
	v_fmac_f32_e32 v131, v229, v137
	s_nop 0
	v_mov_b32_dpp v132, v130 row_shl:4 row_mask:0xf bank_mask:0xf bound_ctrl:1
	v_mov_b32_dpp v133, v131 row_shl:4 row_mask:0xf bank_mask:0xf bound_ctrl:1
	v_fmac_f32_e32 v130, v230, v132
	v_fmac_f32_e32 v131, v230, v133
	v_fma_f32 v130, -v231, v133, v130
	v_fmac_f32_e32 v131, v231, v132
	s_nop 0
	v_mov_b32_dpp v132, v130 row_shl:8 row_mask:0xf bank_mask:0xf bound_ctrl:1
	v_mov_b32_dpp v133, v131 row_shl:8 row_mask:0xf bank_mask:0xf bound_ctrl:1
	v_fmac_f32_e32 v130, v226, v132
	v_fmac_f32_e32 v131, v226, v133
	v_fma_f32 v130, -v227, v133, v130
	v_fmac_f32_e32 v131, v227, v132
	s_nop 0
	v_mov_b32_dpp v128, v130 row_shl:1 row_mask:0xf bank_mask:0xf bound_ctrl:1
	v_mov_b32_dpp v129, v131 row_shl:1 row_mask:0xf bank_mask:0xf bound_ctrl:1
	v_pk_fma_f32 v[130:131], v[196:197], v[110:111], v[120:121] op_sel_hi:[0,1,1]
	v_pk_fma_f32 v[116:117], v[218:219], v[146:147], v[116:117] op_sel_hi:[0,1,1]
	v_pk_fma_f32 v[118:119], v[232:233], v[128:129], v[118:119] op_sel_hi:[0,1,1]
	v_add_u32_e32 v121, s0, v189
	v_cvt_pk_f16_f32 v120, v110, v111
	v_pk_fma_f32 v[122:123], v[212:213], v[126:127], v[122:123] op_sel_hi:[0,1,1]
	v_pk_fma_f32 v[110:111], v[196:197], v[110:111], v[130:131] op_sel:[1,1,0] op_sel_hi:[1,0,1] neg_lo:[1,0,0]
	v_pk_fma_f32 v[130:131], v[218:219], v[146:147], v[116:117] op_sel:[1,1,0] op_sel_hi:[1,0,1] neg_lo:[1,0,0]
	v_pk_fma_f32 v[118:119], v[232:233], v[128:129], v[118:119] op_sel:[1,1,0] op_sel_hi:[1,0,1] neg_lo:[1,0,0]
	v_xor_b32_e32 v121, v121, v188
	v_pk_fma_f32 v[122:123], v[212:213], v[126:127], v[122:123] op_sel:[1,1,0] op_sel_hi:[1,0,1] neg_lo:[1,0,0]
	v_pk_fma_f32 v[116:117], v[196:197], v[110:111], v[104:105] op_sel_hi:[0,1,1]
	v_pk_fma_f32 v[112:113], v[218:219], v[130:131], v[112:113] op_sel_hi:[0,1,1]
	v_pk_fma_f32 v[114:115], v[232:233], v[118:119], v[114:115] op_sel_hi:[0,1,1]
	v_lshl_add_u32 v137, v121, 4, v190
	v_cvt_pk_f16_f32 v104, v110, v111
	v_pk_fma_f32 v[106:107], v[212:213], v[122:123], v[106:107] op_sel_hi:[0,1,1]
	v_pk_fma_f32 v[132:133], v[196:197], v[110:111], v[116:117] op_sel:[1,1,0] op_sel_hi:[1,0,1] neg_lo:[1,0,0]
	v_pk_fma_f32 v[134:135], v[218:219], v[130:131], v[112:113] op_sel:[1,1,0] op_sel_hi:[1,0,1] neg_lo:[1,0,0]
	v_pk_fma_f32 v[144:145], v[232:233], v[118:119], v[114:115] op_sel:[1,1,0] op_sel_hi:[1,0,1] neg_lo:[1,0,0]
	s_nop 0
	s_nop 0
	v_pk_fma_f32 v[106:107], v[212:213], v[122:123], v[106:107] op_sel:[1,1,0] op_sel_hi:[1,0,1] neg_lo:[1,0,0]
	v_pk_fma_f32 v[148:149], v[196:197], v[132:133], v[96:97] op_sel_hi:[0,1,1]
	v_pk_fma_f32 v[100:101], v[218:219], v[134:135], v[100:101] op_sel_hi:[0,1,1]
	v_pk_fma_f32 v[98:99], v[212:213], v[106:107], v[98:99] op_sel_hi:[0,1,1]
	v_pk_fma_f32 v[102:103], v[232:233], v[144:145], v[102:103] op_sel_hi:[0,1,1]
	v_cvt_pk_f16_f32 v96, v132, v133
	v_pk_fma_f32 v[108:109], v[196:197], v[132:133], v[148:149] op_sel:[1,1,0] op_sel_hi:[1,0,1] neg_lo:[1,0,0]
	v_pk_fma_f32 v[132:133], v[218:219], v[134:135], v[100:101] op_sel:[1,1,0] op_sel_hi:[1,0,1] neg_lo:[1,0,0]
	v_pk_fma_f32 v[98:99], v[212:213], v[106:107], v[98:99] op_sel:[1,1,0] op_sel_hi:[1,0,1] neg_lo:[1,0,0]
	v_pk_fma_f32 v[124:125], v[232:233], v[144:145], v[102:103] op_sel:[1,1,0] op_sel_hi:[1,0,1] neg_lo:[1,0,0]
	v_cvt_pk_f16_f32 v100, v108, v109
	v_cvt_pk_f16_f32 v102, v132, v133
	v_cvt_pk_f16_f32 v101, v98, v99
	v_cvt_pk_f16_f32 v103, v124, v125
	v_cvt_pk_f16_f32 v98, v134, v135
	v_cvt_pk_f16_f32 v97, v106, v107
	v_cvt_pk_f16_f32 v99, v144, v145
	v_cvt_pk_f16_f32 v106, v130, v131
	v_cvt_pk_f16_f32 v105, v122, v123
	v_cvt_pk_f16_f32 v107, v118, v119
	v_cvt_pk_f16_f32 v122, v146, v147
	v_cvt_pk_f16_f32 v121, v126, v127
	v_cvt_pk_f16_f32 v123, v128, v129
	s_nop 0
	v_mfma_f32_16x16x32_f16 v[88:91], v[240:243], v[100:103], v[88:91]
	s_add_i32 s0, s0, 4
	v_add_u32_e32 v179, 0x400, v179
	v_add_u32_e32 v174, 0x1000, v174
	v_mfma_f32_16x16x32_f16 v[80:83], v[240:243], v[96:99], v[80:83]
	s_cmp_lg_u32 s0, 16
	v_add_u32_e32 v175, 0x1000, v175
	v_mfma_f32_16x16x32_f16 v[72:75], v[240:243], v[104:107], v[72:75]
	v_mfma_f32_16x16x32_f16 v[64:67], v[240:243], v[120:123], v[64:67]
	s_waitcnt lgkmcnt(0)
	v_mfma_f32_16x16x32_f16 v[56:59], v[244:247], v[100:103], v[56:59]
	v_mfma_f32_16x16x32_f16 v[48:51], v[244:247], v[96:99], v[48:51]
	v_mfma_f32_16x16x32_f16 v[40:43], v[244:247], v[104:107], v[40:43]
	v_mfma_f32_16x16x32_f16 v[32:35], v[244:247], v[120:123], v[32:35]
	s_nop 0
	s_nop 0
	s_waitcnt lgkmcnt(1)
	v_mfma_f32_16x16x32_f16 v[28:31], v[248:251], v[100:103], v[28:31]
	v_mfma_f32_16x16x32_f16 v[24:27], v[248:251], v[96:99], v[24:27]
	v_mfma_f32_16x16x32_f16 v[20:23], v[248:251], v[104:107], v[20:23]
	v_mfma_f32_16x16x32_f16 v[16:19], v[248:251], v[120:123], v[16:19]
	s_waitcnt lgkmcnt(0)
	v_mfma_f32_16x16x32_f16 v[12:15], v[252:255], v[100:103], v[12:15]
	v_mfma_f32_16x16x32_f16 v[8:11], v[252:255], v[96:99], v[8:11]
	v_mfma_f32_16x16x32_f16 v[4:7], v[252:255], v[104:107], v[4:7]
	v_mfma_f32_16x16x32_f16 v[0:3], v[252:255], v[120:123], v[0:3]
	s_cbranch_scc1 .LBB3_47
	s_ashr_i32 s45, s44, 31
	s_lshl_b64 s[0:1], s[44:45], 13
	v_lshl_add_u64 v[38:39], v[138:139], 0, s[0:1]
	s_mov_b32 s1, 0x3f3504f3
	v_mul_f32_e64 v36, |v88|, s1
	s_mov_b32 s3, 0x3ea7ba05
	v_fma_f32 v37, v36, s3, 1.0
	v_rcp_f32_e32 v44, v37
	v_mul_f32_e32 v37, 0xbfb8aa3b, v36
	v_mul_f32_e32 v36, v36, v37
	v_exp_f32_e32 v46, v36
	v_mul_f32_e64 v36, |v89|, s1
	v_fma_f32 v37, v36, s3, 1.0
	v_rcp_f32_e32 v45, v37
	v_mul_f32_e32 v37, 0xbfb8aa3b, v36
	v_mul_f32_e32 v36, v36, v37
	s_mov_b32 s2, 0xbfba00e3
	v_exp_f32_e32 v47, v36
	s_mov_b32 s0, 0x3f87dc22
	v_mov_b64_e32 v[36:37], s[2:3]
	v_pk_fma_f32 v[52:53], v[44:45], s[0:1], v[36:37] op_sel_hi:[1,0,0]
	s_mov_b32 s2, 0x3fb5f0e3
	v_pk_fma_f32 v[52:53], v[44:45], v[52:53], s[2:3] op_sel_hi:[1,1,0]
	s_mov_b32 s4, 0xbe91a98e
	v_pk_fma_f32 v[52:53], v[44:45], v[52:53], s[4:5] op_sel_hi:[1,1,0]
	s_mov_b32 s6, 0x3e827906
	v_pk_fma_f32 v[52:53], v[44:45], v[52:53], s[6:7] op_sel_hi:[1,1,0]
	v_cmp_le_f32_e32 vcc, 0, v89
	v_pk_mul_f32 v[44:45], v[44:45], v[52:53]
	v_mov_b32_e32 v137, 0
	v_pk_mul_f32 v[44:45], v[44:45], 0.5 op_sel_hi:[1,0]
	v_lshl_add_u64 v[38:39], v[38:39], 0, v[136:137]
	v_pk_mul_f32 v[44:45], v[46:47], v[44:45]
	s_nop 0
	v_pk_mul_f32 v[46:47], v[88:89], v[44:45]
	v_pk_fma_f32 v[44:45], v[88:89], v[44:45], v[88:89] neg_lo:[1,0,0] neg_hi:[1,0,0]
	s_nop 0
	v_cndmask_b32_e32 v45, v47, v45, vcc
	v_cmp_le_f32_e32 vcc, 0, v88
	s_nop 1
	v_cndmask_b32_e32 v44, v46, v44, vcc
	v_cvt_pk_f16_f32 v44, v44, v45
	v_mul_f32_e64 v45, |v90|, s1
	v_mul_f32_e32 v47, 0xbfb8aa3b, v45
	v_fma_f32 v46, v45, s3, 1.0
	v_mul_f32_e32 v45, v45, v47
	v_exp_f32_e32 v52, v45
	v_mul_f32_e64 v45, |v91|, s1
	v_fma_f32 v47, v45, s3, 1.0
	v_rcp_f32_e32 v46, v46
	v_rcp_f32_e32 v47, v47
	v_mul_f32_e32 v53, 0xbfb8aa3b, v45
	v_mul_f32_e32 v45, v45, v53
	v_exp_f32_e32 v53, v45
	v_pk_fma_f32 v[54:55], v[46:47], s[0:1], v[36:37] op_sel_hi:[1,0,0]
	v_cmp_le_f32_e32 vcc, 0, v91
	v_pk_fma_f32 v[54:55], v[46:47], v[54:55], s[2:3] op_sel_hi:[1,1,0]
	s_nop 0
	v_pk_fma_f32 v[54:55], v[46:47], v[54:55], s[4:5] op_sel_hi:[1,1,0]
	s_nop 0
	v_pk_fma_f32 v[54:55], v[46:47], v[54:55], s[6:7] op_sel_hi:[1,1,0]
	s_nop 0
	v_pk_mul_f32 v[46:47], v[46:47], v[54:55]
	s_nop 0
	v_pk_mul_f32 v[46:47], v[46:47], 0.5 op_sel_hi:[1,0]
	s_nop 0
	v_pk_mul_f32 v[46:47], v[52:53], v[46:47]
	s_nop 0
	v_pk_mul_f32 v[52:53], v[90:91], v[46:47]
	v_pk_fma_f32 v[46:47], v[90:91], v[46:47], v[90:91] neg_lo:[1,0,0] neg_hi:[1,0,0]
	s_nop 0
	v_cndmask_b32_e32 v45, v53, v47, vcc
	v_cmp_le_f32_e32 vcc, 0, v90
	v_mul_f32_e64 v47, |v81|, s1
	s_nop 0
	v_cndmask_b32_e32 v46, v52, v46, vcc
	v_cvt_pk_f16_f32 v45, v46, v45
	global_store_dwordx2 v[38:39], v[44:45], off
	v_mul_f32_e64 v45, |v80|, s1
	v_mul_f32_e32 v46, 0xbfb8aa3b, v45
	v_fma_f32 v44, v45, s3, 1.0
	v_mul_f32_e32 v45, v45, v46
	v_exp_f32_e32 v46, v45
	v_fma_f32 v45, v47, s3, 1.0
	v_rcp_f32_e32 v44, v44
	v_rcp_f32_e32 v45, v45
	v_mul_f32_e32 v52, 0xbfb8aa3b, v47
	v_mul_f32_e32 v47, v47, v52
	v_exp_f32_e32 v47, v47
	v_pk_fma_f32 v[52:53], v[44:45], s[0:1], v[36:37] op_sel_hi:[1,0,0]
	v_cmp_le_f32_e32 vcc, 0, v81
	v_pk_fma_f32 v[52:53], v[44:45], v[52:53], s[2:3] op_sel_hi:[1,1,0]
	s_nop 0
	v_pk_fma_f32 v[52:53], v[44:45], v[52:53], s[4:5] op_sel_hi:[1,1,0]
	s_nop 0
	v_pk_fma_f32 v[52:53], v[44:45], v[52:53], s[6:7] op_sel_hi:[1,1,0]
	s_nop 0
	v_pk_mul_f32 v[44:45], v[44:45], v[52:53]
	s_nop 0
	v_pk_mul_f32 v[44:45], v[44:45], 0.5 op_sel_hi:[1,0]
	s_nop 0
	v_pk_mul_f32 v[44:45], v[46:47], v[44:45]
	s_nop 0
	v_pk_mul_f32 v[46:47], v[80:81], v[44:45]
	v_pk_fma_f32 v[44:45], v[80:81], v[44:45], v[80:81] neg_lo:[1,0,0] neg_hi:[1,0,0]
	s_nop 0
	v_cndmask_b32_e32 v45, v47, v45, vcc
	v_cmp_le_f32_e32 vcc, 0, v80
	s_nop 1
	v_cndmask_b32_e32 v44, v46, v44, vcc
	v_cvt_pk_f16_f32 v44, v44, v45
	v_mul_f32_e64 v45, |v82|, s1
	v_mul_f32_e32 v47, 0xbfb8aa3b, v45
	v_fma_f32 v46, v45, s3, 1.0
	v_mul_f32_e32 v45, v45, v47
	v_exp_f32_e32 v52, v45
	v_mul_f32_e64 v45, |v83|, s1
	v_fma_f32 v47, v45, s3, 1.0
	v_rcp_f32_e32 v46, v46
	v_rcp_f32_e32 v47, v47
	v_mul_f32_e32 v53, 0xbfb8aa3b, v45
	v_mul_f32_e32 v45, v45, v53
	v_exp_f32_e32 v53, v45
	v_pk_fma_f32 v[54:55], v[46:47], s[0:1], v[36:37] op_sel_hi:[1,0,0]
	v_cmp_le_f32_e32 vcc, 0, v83
	v_pk_fma_f32 v[54:55], v[46:47], v[54:55], s[2:3] op_sel_hi:[1,1,0]
	s_nop 0
	v_pk_fma_f32 v[54:55], v[46:47], v[54:55], s[4:5] op_sel_hi:[1,1,0]
	s_nop 0
	v_pk_fma_f32 v[54:55], v[46:47], v[54:55], s[6:7] op_sel_hi:[1,1,0]
	s_nop 0
	v_pk_mul_f32 v[46:47], v[46:47], v[54:55]
	s_nop 0
	v_pk_mul_f32 v[46:47], v[46:47], 0.5 op_sel_hi:[1,0]
	s_nop 0
	v_pk_mul_f32 v[46:47], v[52:53], v[46:47]
	s_nop 0
	v_pk_mul_f32 v[52:53], v[82:83], v[46:47]
	v_pk_fma_f32 v[46:47], v[82:83], v[46:47], v[82:83] neg_lo:[1,0,0] neg_hi:[1,0,0]
	s_nop 0
	v_cndmask_b32_e32 v45, v53, v47, vcc
	v_cmp_le_f32_e32 vcc, 0, v82
	v_mul_f32_e64 v47, |v73|, s1
	s_nop 0
	v_cndmask_b32_e32 v46, v52, v46, vcc
	v_cvt_pk_f16_f32 v45, v46, v45
	global_store_dwordx2 v[38:39], v[44:45], off offset:128
	v_mul_f32_e64 v45, |v72|, s1
	v_mul_f32_e32 v46, 0xbfb8aa3b, v45
	v_fma_f32 v44, v45, s3, 1.0
	v_mul_f32_e32 v45, v45, v46
	v_exp_f32_e32 v46, v45
	v_fma_f32 v45, v47, s3, 1.0
	v_rcp_f32_e32 v44, v44
	v_rcp_f32_e32 v45, v45
	v_mul_f32_e32 v52, 0xbfb8aa3b, v47
	v_mul_f32_e32 v47, v47, v52
	v_exp_f32_e32 v47, v47
	v_pk_fma_f32 v[52:53], v[44:45], s[0:1], v[36:37] op_sel_hi:[1,0,0]
	v_cmp_le_f32_e32 vcc, 0, v73
	v_pk_fma_f32 v[52:53], v[44:45], v[52:53], s[2:3] op_sel_hi:[1,1,0]
	s_nop 0
	v_pk_fma_f32 v[52:53], v[44:45], v[52:53], s[4:5] op_sel_hi:[1,1,0]
	s_nop 0
	v_pk_fma_f32 v[52:53], v[44:45], v[52:53], s[6:7] op_sel_hi:[1,1,0]
	s_nop 0
	v_pk_mul_f32 v[44:45], v[44:45], v[52:53]
	s_nop 0
	v_pk_mul_f32 v[44:45], v[44:45], 0.5 op_sel_hi:[1,0]
	s_nop 0
	v_pk_mul_f32 v[44:45], v[46:47], v[44:45]
	s_nop 0
	v_pk_mul_f32 v[46:47], v[72:73], v[44:45]
	v_pk_fma_f32 v[44:45], v[72:73], v[44:45], v[72:73] neg_lo:[1,0,0] neg_hi:[1,0,0]
	s_nop 0
	v_cndmask_b32_e32 v45, v47, v45, vcc
	v_cmp_le_f32_e32 vcc, 0, v72
	s_nop 1
	v_cndmask_b32_e32 v44, v46, v44, vcc
	v_cvt_pk_f16_f32 v44, v44, v45
	v_mul_f32_e64 v45, |v74|, s1
	v_mul_f32_e32 v47, 0xbfb8aa3b, v45
	v_fma_f32 v46, v45, s3, 1.0
	v_mul_f32_e32 v45, v45, v47
	v_exp_f32_e32 v52, v45
	v_mul_f32_e64 v45, |v75|, s1
	v_fma_f32 v47, v45, s3, 1.0
	v_rcp_f32_e32 v46, v46
	v_rcp_f32_e32 v47, v47
	v_mul_f32_e32 v53, 0xbfb8aa3b, v45
	v_mul_f32_e32 v45, v45, v53
	v_exp_f32_e32 v53, v45
	v_pk_fma_f32 v[54:55], v[46:47], s[0:1], v[36:37] op_sel_hi:[1,0,0]
	v_cmp_le_f32_e32 vcc, 0, v75
	v_pk_fma_f32 v[54:55], v[46:47], v[54:55], s[2:3] op_sel_hi:[1,1,0]
	s_nop 0
	v_pk_fma_f32 v[54:55], v[46:47], v[54:55], s[4:5] op_sel_hi:[1,1,0]
	s_nop 0
	v_pk_fma_f32 v[54:55], v[46:47], v[54:55], s[6:7] op_sel_hi:[1,1,0]
	s_nop 0
	v_pk_mul_f32 v[46:47], v[46:47], v[54:55]
	s_nop 0
	v_pk_mul_f32 v[46:47], v[46:47], 0.5 op_sel_hi:[1,0]
	s_nop 0
	v_pk_mul_f32 v[46:47], v[52:53], v[46:47]
	s_nop 0
	v_pk_mul_f32 v[52:53], v[74:75], v[46:47]
	v_pk_fma_f32 v[46:47], v[74:75], v[46:47], v[74:75] neg_lo:[1,0,0] neg_hi:[1,0,0]
	s_nop 0
	v_cndmask_b32_e32 v45, v53, v47, vcc
	v_cmp_le_f32_e32 vcc, 0, v74
	v_mul_f32_e64 v47, |v65|, s1
	s_nop 0
	v_cndmask_b32_e32 v46, v52, v46, vcc
	v_cvt_pk_f16_f32 v45, v46, v45
	global_store_dwordx2 v[38:39], v[44:45], off offset:256
	v_mul_f32_e64 v45, |v64|, s1
	v_mul_f32_e32 v46, 0xbfb8aa3b, v45
	v_fma_f32 v44, v45, s3, 1.0
	v_mul_f32_e32 v45, v45, v46
	v_exp_f32_e32 v46, v45
	v_fma_f32 v45, v47, s3, 1.0
	v_rcp_f32_e32 v44, v44
	v_rcp_f32_e32 v45, v45
	v_mul_f32_e32 v52, 0xbfb8aa3b, v47
	v_mul_f32_e32 v47, v47, v52
	v_exp_f32_e32 v47, v47
	v_pk_fma_f32 v[52:53], v[44:45], s[0:1], v[36:37] op_sel_hi:[1,0,0]
	v_cmp_le_f32_e32 vcc, 0, v65
	v_pk_fma_f32 v[52:53], v[44:45], v[52:53], s[2:3] op_sel_hi:[1,1,0]
	s_nop 0
	v_pk_fma_f32 v[52:53], v[44:45], v[52:53], s[4:5] op_sel_hi:[1,1,0]
	s_nop 0
	v_pk_fma_f32 v[52:53], v[44:45], v[52:53], s[6:7] op_sel_hi:[1,1,0]
	s_nop 0
	v_pk_mul_f32 v[44:45], v[44:45], v[52:53]
	s_nop 0
	v_pk_mul_f32 v[44:45], v[44:45], 0.5 op_sel_hi:[1,0]
	s_nop 0
	v_pk_mul_f32 v[44:45], v[46:47], v[44:45]
	s_nop 0
	v_pk_mul_f32 v[46:47], v[64:65], v[44:45]
	v_pk_fma_f32 v[44:45], v[64:65], v[44:45], v[64:65] neg_lo:[1,0,0] neg_hi:[1,0,0]
	s_nop 0
	v_cndmask_b32_e32 v45, v47, v45, vcc
	v_cmp_le_f32_e32 vcc, 0, v64
	s_nop 1
	v_cndmask_b32_e32 v44, v46, v44, vcc
	v_cvt_pk_f16_f32 v44, v44, v45
	v_mul_f32_e64 v45, |v66|, s1
	v_mul_f32_e32 v47, 0xbfb8aa3b, v45
	v_fma_f32 v46, v45, s3, 1.0
	v_mul_f32_e32 v45, v45, v47
	v_exp_f32_e32 v52, v45
	v_mul_f32_e64 v45, |v67|, s1
	v_fma_f32 v47, v45, s3, 1.0
	v_rcp_f32_e32 v46, v46
	v_rcp_f32_e32 v47, v47
	v_mul_f32_e32 v53, 0xbfb8aa3b, v45
	v_mul_f32_e32 v45, v45, v53
	v_exp_f32_e32 v53, v45
	v_pk_fma_f32 v[54:55], v[46:47], s[0:1], v[36:37] op_sel_hi:[1,0,0]
	v_cmp_le_f32_e32 vcc, 0, v67
	v_pk_fma_f32 v[54:55], v[46:47], v[54:55], s[2:3] op_sel_hi:[1,1,0]
	s_nop 0
	v_pk_fma_f32 v[54:55], v[46:47], v[54:55], s[4:5] op_sel_hi:[1,1,0]
	s_nop 0
	v_pk_fma_f32 v[54:55], v[46:47], v[54:55], s[6:7] op_sel_hi:[1,1,0]
	s_nop 0
	v_pk_mul_f32 v[46:47], v[46:47], v[54:55]
	s_nop 0
	v_pk_mul_f32 v[46:47], v[46:47], 0.5 op_sel_hi:[1,0]
	s_nop 0
	v_pk_mul_f32 v[46:47], v[52:53], v[46:47]
	s_nop 0
	v_pk_mul_f32 v[52:53], v[66:67], v[46:47]
	v_pk_fma_f32 v[46:47], v[66:67], v[46:47], v[66:67] neg_lo:[1,0,0] neg_hi:[1,0,0]
	s_nop 0
	v_cndmask_b32_e32 v45, v53, v47, vcc
	v_cmp_le_f32_e32 vcc, 0, v66
	v_mul_f32_e64 v47, |v57|, s1
	s_nop 0
	v_cndmask_b32_e32 v46, v52, v46, vcc
	v_cvt_pk_f16_f32 v45, v46, v45
	global_store_dwordx2 v[38:39], v[44:45], off offset:384
	v_mul_f32_e64 v45, |v56|, s1
	v_mul_f32_e32 v46, 0xbfb8aa3b, v45
	v_fma_f32 v44, v45, s3, 1.0
	v_mul_f32_e32 v45, v45, v46
	v_exp_f32_e32 v46, v45
	v_fma_f32 v45, v47, s3, 1.0
	v_rcp_f32_e32 v44, v44
	v_rcp_f32_e32 v45, v45
	v_mul_f32_e32 v52, 0xbfb8aa3b, v47
	v_mul_f32_e32 v47, v47, v52
	v_exp_f32_e32 v47, v47
	v_pk_fma_f32 v[52:53], v[44:45], s[0:1], v[36:37] op_sel_hi:[1,0,0]
	v_cmp_le_f32_e32 vcc, 0, v57
	v_pk_fma_f32 v[52:53], v[44:45], v[52:53], s[2:3] op_sel_hi:[1,1,0]
	s_nop 0
	v_pk_fma_f32 v[52:53], v[44:45], v[52:53], s[4:5] op_sel_hi:[1,1,0]
	s_nop 0
	v_pk_fma_f32 v[52:53], v[44:45], v[52:53], s[6:7] op_sel_hi:[1,1,0]
	s_nop 0
	v_pk_mul_f32 v[44:45], v[44:45], v[52:53]
	s_nop 0
	v_pk_mul_f32 v[44:45], v[44:45], 0.5 op_sel_hi:[1,0]
	s_nop 0
	v_pk_mul_f32 v[44:45], v[46:47], v[44:45]
	s_nop 0
	v_pk_mul_f32 v[46:47], v[56:57], v[44:45]
	v_pk_fma_f32 v[44:45], v[56:57], v[44:45], v[56:57] neg_lo:[1,0,0] neg_hi:[1,0,0]
	s_nop 0
	v_cndmask_b32_e32 v45, v47, v45, vcc
	v_cmp_le_f32_e32 vcc, 0, v56
	s_nop 1
	v_cndmask_b32_e32 v44, v46, v44, vcc
	v_cvt_pk_f16_f32 v44, v44, v45
	v_mul_f32_e64 v45, |v58|, s1
	v_mul_f32_e32 v47, 0xbfb8aa3b, v45
	v_fma_f32 v46, v45, s3, 1.0
	v_mul_f32_e32 v45, v45, v47
	v_exp_f32_e32 v52, v45
	v_mul_f32_e64 v45, |v59|, s1
	v_fma_f32 v47, v45, s3, 1.0
	v_rcp_f32_e32 v46, v46
	v_rcp_f32_e32 v47, v47
	v_mul_f32_e32 v53, 0xbfb8aa3b, v45
	v_mul_f32_e32 v45, v45, v53
	v_exp_f32_e32 v53, v45
	v_pk_fma_f32 v[54:55], v[46:47], s[0:1], v[36:37] op_sel_hi:[1,0,0]
	v_cmp_le_f32_e32 vcc, 0, v59
	v_pk_fma_f32 v[54:55], v[46:47], v[54:55], s[2:3] op_sel_hi:[1,1,0]
	s_nop 0
	v_pk_fma_f32 v[54:55], v[46:47], v[54:55], s[4:5] op_sel_hi:[1,1,0]
	s_nop 0
	v_pk_fma_f32 v[54:55], v[46:47], v[54:55], s[6:7] op_sel_hi:[1,1,0]
	s_nop 0
	v_pk_mul_f32 v[46:47], v[46:47], v[54:55]
	s_nop 0
	v_pk_mul_f32 v[46:47], v[46:47], 0.5 op_sel_hi:[1,0]
	s_nop 0
	v_pk_mul_f32 v[46:47], v[52:53], v[46:47]
	s_nop 0
	v_pk_mul_f32 v[52:53], v[58:59], v[46:47]
	v_pk_fma_f32 v[46:47], v[58:59], v[46:47], v[58:59] neg_lo:[1,0,0] neg_hi:[1,0,0]
	s_nop 0
	v_cndmask_b32_e32 v45, v53, v47, vcc
	v_cmp_le_f32_e32 vcc, 0, v58
	v_mul_f32_e64 v47, |v49|, s1
	s_nop 0
	v_cndmask_b32_e32 v46, v52, v46, vcc
	v_cvt_pk_f16_f32 v45, v46, v45
	global_store_dwordx2 v[38:39], v[44:45], off offset:32
	v_mul_f32_e64 v45, |v48|, s1
	v_mul_f32_e32 v46, 0xbfb8aa3b, v45
	v_fma_f32 v44, v45, s3, 1.0
	v_mul_f32_e32 v45, v45, v46
	v_exp_f32_e32 v46, v45
	v_fma_f32 v45, v47, s3, 1.0
	v_rcp_f32_e32 v44, v44
	v_rcp_f32_e32 v45, v45
	v_mul_f32_e32 v52, 0xbfb8aa3b, v47
	v_mul_f32_e32 v47, v47, v52
	v_exp_f32_e32 v47, v47
	v_pk_fma_f32 v[52:53], v[44:45], s[0:1], v[36:37] op_sel_hi:[1,0,0]
	v_cmp_le_f32_e32 vcc, 0, v49
	v_pk_fma_f32 v[52:53], v[44:45], v[52:53], s[2:3] op_sel_hi:[1,1,0]
	s_nop 0
	v_pk_fma_f32 v[52:53], v[44:45], v[52:53], s[4:5] op_sel_hi:[1,1,0]
	s_nop 0
	v_pk_fma_f32 v[52:53], v[44:45], v[52:53], s[6:7] op_sel_hi:[1,1,0]
	s_nop 0
	v_pk_mul_f32 v[44:45], v[44:45], v[52:53]
	s_nop 0
	v_pk_mul_f32 v[44:45], v[44:45], 0.5 op_sel_hi:[1,0]
	s_nop 0
	v_pk_mul_f32 v[44:45], v[46:47], v[44:45]
	s_nop 0
	v_pk_mul_f32 v[46:47], v[48:49], v[44:45]
	v_pk_fma_f32 v[44:45], v[48:49], v[44:45], v[48:49] neg_lo:[1,0,0] neg_hi:[1,0,0]
	s_nop 0
	v_cndmask_b32_e32 v45, v47, v45, vcc
	v_cmp_le_f32_e32 vcc, 0, v48
	s_nop 1
	v_cndmask_b32_e32 v44, v46, v44, vcc
	v_cvt_pk_f16_f32 v44, v44, v45
	v_mul_f32_e64 v45, |v50|, s1
	v_mul_f32_e32 v47, 0xbfb8aa3b, v45
	v_fma_f32 v46, v45, s3, 1.0
	v_mul_f32_e32 v45, v45, v47
	v_exp_f32_e32 v48, v45
	v_mul_f32_e64 v45, |v51|, s1
	v_fma_f32 v47, v45, s3, 1.0
	v_rcp_f32_e32 v46, v46
	v_rcp_f32_e32 v47, v47
	v_mul_f32_e32 v49, 0xbfb8aa3b, v45
	v_mul_f32_e32 v45, v45, v49
	v_exp_f32_e32 v49, v45
	v_pk_fma_f32 v[52:53], v[46:47], s[0:1], v[36:37] op_sel_hi:[1,0,0]
	v_cmp_le_f32_e32 vcc, 0, v51
	v_pk_fma_f32 v[52:53], v[46:47], v[52:53], s[2:3] op_sel_hi:[1,1,0]
	s_nop 0
	v_pk_fma_f32 v[52:53], v[46:47], v[52:53], s[4:5] op_sel_hi:[1,1,0]
	s_nop 0
	v_pk_fma_f32 v[52:53], v[46:47], v[52:53], s[6:7] op_sel_hi:[1,1,0]
	s_nop 0
	v_pk_mul_f32 v[46:47], v[46:47], v[52:53]
	s_nop 0
	v_pk_mul_f32 v[46:47], v[46:47], 0.5 op_sel_hi:[1,0]
	s_nop 0
	v_pk_mul_f32 v[46:47], v[48:49], v[46:47]
	s_nop 0
	v_pk_mul_f32 v[48:49], v[50:51], v[46:47]
	v_pk_fma_f32 v[46:47], v[50:51], v[46:47], v[50:51] neg_lo:[1,0,0] neg_hi:[1,0,0]
	s_nop 0
	v_cndmask_b32_e32 v45, v49, v47, vcc
	v_cmp_le_f32_e32 vcc, 0, v50
	v_mul_f32_e64 v47, |v41|, s1
	s_nop 0
	v_cndmask_b32_e32 v46, v48, v46, vcc
	v_cvt_pk_f16_f32 v45, v46, v45
	global_store_dwordx2 v[38:39], v[44:45], off offset:160
	v_mul_f32_e64 v45, |v40|, s1
	v_mul_f32_e32 v46, 0xbfb8aa3b, v45
	v_fma_f32 v44, v45, s3, 1.0
	v_mul_f32_e32 v45, v45, v46
	v_exp_f32_e32 v46, v45
	v_fma_f32 v45, v47, s3, 1.0
	v_rcp_f32_e32 v44, v44
	v_rcp_f32_e32 v45, v45
	v_mul_f32_e32 v48, 0xbfb8aa3b, v47
	v_mul_f32_e32 v47, v47, v48
	v_exp_f32_e32 v47, v47
	v_pk_fma_f32 v[48:49], v[44:45], s[0:1], v[36:37] op_sel_hi:[1,0,0]
	v_cmp_le_f32_e32 vcc, 0, v41
	v_pk_fma_f32 v[48:49], v[44:45], v[48:49], s[2:3] op_sel_hi:[1,1,0]
	s_nop 0
	v_pk_fma_f32 v[48:49], v[44:45], v[48:49], s[4:5] op_sel_hi:[1,1,0]
	s_nop 0
	v_pk_fma_f32 v[48:49], v[44:45], v[48:49], s[6:7] op_sel_hi:[1,1,0]
	s_nop 0
	v_pk_mul_f32 v[44:45], v[44:45], v[48:49]
	s_nop 0
	v_pk_mul_f32 v[44:45], v[44:45], 0.5 op_sel_hi:[1,0]
	s_nop 0
	v_pk_mul_f32 v[44:45], v[46:47], v[44:45]
	s_nop 0
	v_pk_mul_f32 v[46:47], v[40:41], v[44:45]
	v_pk_fma_f32 v[44:45], v[40:41], v[44:45], v[40:41] neg_lo:[1,0,0] neg_hi:[1,0,0]
	s_nop 0
	v_cndmask_b32_e32 v41, v47, v45, vcc
	v_cmp_le_f32_e32 vcc, 0, v40
	s_nop 1
	v_cndmask_b32_e32 v40, v46, v44, vcc
	v_cvt_pk_f16_f32 v40, v40, v41
	v_mul_f32_e64 v41, |v42|, s1
	v_mul_f32_e32 v45, 0xbfb8aa3b, v41
	v_fma_f32 v44, v41, s3, 1.0
	v_mul_f32_e32 v41, v41, v45
	v_exp_f32_e32 v46, v41
	v_mul_f32_e64 v41, |v43|, s1
	v_fma_f32 v45, v41, s3, 1.0
	v_rcp_f32_e32 v44, v44
	v_rcp_f32_e32 v45, v45
	v_mul_f32_e32 v47, 0xbfb8aa3b, v41
	v_mul_f32_e32 v41, v41, v47
	v_exp_f32_e32 v47, v41
	v_pk_fma_f32 v[48:49], v[44:45], s[0:1], v[36:37] op_sel_hi:[1,0,0]
	v_cmp_le_f32_e32 vcc, 0, v43
	v_pk_fma_f32 v[48:49], v[44:45], v[48:49], s[2:3] op_sel_hi:[1,1,0]
	s_nop 0
	v_pk_fma_f32 v[48:49], v[44:45], v[48:49], s[4:5] op_sel_hi:[1,1,0]
	s_nop 0
	v_pk_fma_f32 v[48:49], v[44:45], v[48:49], s[6:7] op_sel_hi:[1,1,0]
	s_nop 0
	v_pk_mul_f32 v[44:45], v[44:45], v[48:49]
	s_nop 0
	v_pk_mul_f32 v[44:45], v[44:45], 0.5 op_sel_hi:[1,0]
	s_nop 0
	v_pk_mul_f32 v[44:45], v[46:47], v[44:45]
	s_nop 0
	v_pk_mul_f32 v[46:47], v[42:43], v[44:45]
	v_pk_fma_f32 v[44:45], v[42:43], v[44:45], v[42:43] neg_lo:[1,0,0] neg_hi:[1,0,0]
	v_mul_f32_e64 v43, |v33|, s1
	v_cndmask_b32_e32 v41, v47, v45, vcc
	v_cmp_le_f32_e32 vcc, 0, v42
	s_nop 1
	v_cndmask_b32_e32 v42, v46, v44, vcc
	v_cvt_pk_f16_f32 v41, v42, v41
	global_store_dwordx2 v[38:39], v[40:41], off offset:288
	v_mul_f32_e64 v41, |v32|, s1
	v_mul_f32_e32 v42, 0xbfb8aa3b, v41
	v_fma_f32 v40, v41, s3, 1.0
	v_mul_f32_e32 v41, v41, v42
	v_exp_f32_e32 v42, v41
	v_fma_f32 v41, v43, s3, 1.0
	v_rcp_f32_e32 v40, v40
	v_rcp_f32_e32 v41, v41
	v_mul_f32_e32 v44, 0xbfb8aa3b, v43
	v_mul_f32_e32 v43, v43, v44
	v_exp_f32_e32 v43, v43
	v_pk_fma_f32 v[44:45], v[40:41], s[0:1], v[36:37] op_sel_hi:[1,0,0]
	v_cmp_le_f32_e32 vcc, 0, v33
	v_pk_fma_f32 v[44:45], v[40:41], v[44:45], s[2:3] op_sel_hi:[1,1,0]
	s_nop 0
	v_pk_fma_f32 v[44:45], v[40:41], v[44:45], s[4:5] op_sel_hi:[1,1,0]
	s_nop 0
	v_pk_fma_f32 v[44:45], v[40:41], v[44:45], s[6:7] op_sel_hi:[1,1,0]
	s_nop 0
	v_pk_mul_f32 v[40:41], v[40:41], v[44:45]
	s_nop 0
	v_pk_mul_f32 v[40:41], v[40:41], 0.5 op_sel_hi:[1,0]
	s_nop 0
	v_pk_mul_f32 v[40:41], v[42:43], v[40:41]
	s_nop 0
	v_pk_mul_f32 v[42:43], v[32:33], v[40:41]
	v_pk_fma_f32 v[40:41], v[32:33], v[40:41], v[32:33] neg_lo:[1,0,0] neg_hi:[1,0,0]
	s_nop 0
	v_cndmask_b32_e32 v33, v43, v41, vcc
	v_cmp_le_f32_e32 vcc, 0, v32
	s_nop 1
	v_cndmask_b32_e32 v32, v42, v40, vcc
	v_cvt_pk_f16_f32 v32, v32, v33
	v_mul_f32_e64 v33, |v34|, s1
	v_mul_f32_e32 v41, 0xbfb8aa3b, v33
	v_fma_f32 v40, v33, s3, 1.0
	v_mul_f32_e32 v33, v33, v41
	v_exp_f32_e32 v42, v33
	v_mul_f32_e64 v33, |v35|, s1
	v_fma_f32 v41, v33, s3, 1.0
	v_rcp_f32_e32 v40, v40
	v_rcp_f32_e32 v41, v41
	v_mul_f32_e32 v43, 0xbfb8aa3b, v33
	v_mul_f32_e32 v33, v33, v43
	v_exp_f32_e32 v43, v33
	v_pk_fma_f32 v[44:45], v[40:41], s[0:1], v[36:37] op_sel_hi:[1,0,0]
	v_cmp_le_f32_e32 vcc, 0, v35
	v_pk_fma_f32 v[44:45], v[40:41], v[44:45], s[2:3] op_sel_hi:[1,1,0]
	s_nop 0
	v_pk_fma_f32 v[44:45], v[40:41], v[44:45], s[4:5] op_sel_hi:[1,1,0]
	s_nop 0
	v_pk_fma_f32 v[44:45], v[40:41], v[44:45], s[6:7] op_sel_hi:[1,1,0]
	s_nop 0
	v_pk_mul_f32 v[40:41], v[40:41], v[44:45]
	s_nop 0
	v_pk_mul_f32 v[40:41], v[40:41], 0.5 op_sel_hi:[1,0]
	s_nop 0
	v_pk_mul_f32 v[40:41], v[42:43], v[40:41]
	s_nop 0
	v_pk_mul_f32 v[42:43], v[34:35], v[40:41]
	v_pk_fma_f32 v[40:41], v[34:35], v[40:41], v[34:35] neg_lo:[1,0,0] neg_hi:[1,0,0]
	v_mul_f32_e64 v35, |v29|, s1
	v_cndmask_b32_e32 v33, v43, v41, vcc
	v_cmp_le_f32_e32 vcc, 0, v34
	s_nop 1
	v_cndmask_b32_e32 v34, v42, v40, vcc
	v_cvt_pk_f16_f32 v33, v34, v33
	global_store_dwordx2 v[38:39], v[32:33], off offset:416
	v_mul_f32_e64 v33, |v28|, s1
	v_mul_f32_e32 v34, 0xbfb8aa3b, v33
	v_fma_f32 v32, v33, s3, 1.0
	v_mul_f32_e32 v33, v33, v34
	v_exp_f32_e32 v34, v33
	v_fma_f32 v33, v35, s3, 1.0
	v_rcp_f32_e32 v32, v32
	v_rcp_f32_e32 v33, v33
	v_mul_f32_e32 v40, 0xbfb8aa3b, v35
	v_mul_f32_e32 v35, v35, v40
	v_exp_f32_e32 v35, v35
	v_pk_fma_f32 v[40:41], v[32:33], s[0:1], v[36:37] op_sel_hi:[1,0,0]
	v_cmp_le_f32_e32 vcc, 0, v29
	v_pk_fma_f32 v[40:41], v[32:33], v[40:41], s[2:3] op_sel_hi:[1,1,0]
	s_nop 0
	v_pk_fma_f32 v[40:41], v[32:33], v[40:41], s[4:5] op_sel_hi:[1,1,0]
	s_nop 0
	v_pk_fma_f32 v[40:41], v[32:33], v[40:41], s[6:7] op_sel_hi:[1,1,0]
	s_nop 0
	v_pk_mul_f32 v[32:33], v[32:33], v[40:41]
	s_nop 0
	v_pk_mul_f32 v[32:33], v[32:33], 0.5 op_sel_hi:[1,0]
	s_nop 0
	v_pk_mul_f32 v[32:33], v[34:35], v[32:33]
	s_nop 0
	v_pk_mul_f32 v[34:35], v[28:29], v[32:33]
	v_pk_fma_f32 v[32:33], v[28:29], v[32:33], v[28:29] neg_lo:[1,0,0] neg_hi:[1,0,0]
	s_nop 0
	v_cndmask_b32_e32 v29, v35, v33, vcc
	v_cmp_le_f32_e32 vcc, 0, v28
	s_nop 1
	v_cndmask_b32_e32 v28, v34, v32, vcc
	v_cvt_pk_f16_f32 v28, v28, v29
	v_mul_f32_e64 v29, |v30|, s1
	v_mul_f32_e32 v33, 0xbfb8aa3b, v29
	v_fma_f32 v32, v29, s3, 1.0
	v_mul_f32_e32 v29, v29, v33
	v_exp_f32_e32 v34, v29
	v_mul_f32_e64 v29, |v31|, s1
	v_fma_f32 v33, v29, s3, 1.0
	v_rcp_f32_e32 v32, v32
	v_rcp_f32_e32 v33, v33
	v_mul_f32_e32 v35, 0xbfb8aa3b, v29
	v_mul_f32_e32 v29, v29, v35
	v_exp_f32_e32 v35, v29
	v_pk_fma_f32 v[40:41], v[32:33], s[0:1], v[36:37] op_sel_hi:[1,0,0]
	v_cmp_le_f32_e32 vcc, 0, v31
	v_pk_fma_f32 v[40:41], v[32:33], v[40:41], s[2:3] op_sel_hi:[1,1,0]
	s_nop 0
	v_pk_fma_f32 v[40:41], v[32:33], v[40:41], s[4:5] op_sel_hi:[1,1,0]
	s_nop 0
	v_pk_fma_f32 v[40:41], v[32:33], v[40:41], s[6:7] op_sel_hi:[1,1,0]
	s_nop 0
	v_pk_mul_f32 v[32:33], v[32:33], v[40:41]
	s_nop 0
	v_pk_mul_f32 v[32:33], v[32:33], 0.5 op_sel_hi:[1,0]
	s_nop 0
	v_pk_mul_f32 v[32:33], v[34:35], v[32:33]
	s_nop 0
	v_pk_mul_f32 v[34:35], v[30:31], v[32:33]
	v_pk_fma_f32 v[32:33], v[30:31], v[32:33], v[30:31] neg_lo:[1,0,0] neg_hi:[1,0,0]
	v_mul_f32_e64 v31, |v25|, s1
	v_cndmask_b32_e32 v29, v35, v33, vcc
	v_cmp_le_f32_e32 vcc, 0, v30
	s_nop 1
	v_cndmask_b32_e32 v30, v34, v32, vcc
	v_cvt_pk_f16_f32 v29, v30, v29
	global_store_dwordx2 v[38:39], v[28:29], off offset:64
	v_mul_f32_e64 v29, |v24|, s1
	v_mul_f32_e32 v30, 0xbfb8aa3b, v29
	v_fma_f32 v28, v29, s3, 1.0
	v_mul_f32_e32 v29, v29, v30
	v_exp_f32_e32 v30, v29
	v_fma_f32 v29, v31, s3, 1.0
	v_rcp_f32_e32 v28, v28
	v_rcp_f32_e32 v29, v29
	v_mul_f32_e32 v32, 0xbfb8aa3b, v31
	v_mul_f32_e32 v31, v31, v32
	v_exp_f32_e32 v31, v31
	v_pk_fma_f32 v[32:33], v[28:29], s[0:1], v[36:37] op_sel_hi:[1,0,0]
	v_cmp_le_f32_e32 vcc, 0, v25
	v_pk_fma_f32 v[32:33], v[28:29], v[32:33], s[2:3] op_sel_hi:[1,1,0]
	s_nop 0
	v_pk_fma_f32 v[32:33], v[28:29], v[32:33], s[4:5] op_sel_hi:[1,1,0]
	s_nop 0
	v_pk_fma_f32 v[32:33], v[28:29], v[32:33], s[6:7] op_sel_hi:[1,1,0]
	s_nop 0
	v_pk_mul_f32 v[28:29], v[28:29], v[32:33]
	s_nop 0
	v_pk_mul_f32 v[28:29], v[28:29], 0.5 op_sel_hi:[1,0]
	s_nop 0
	v_pk_mul_f32 v[28:29], v[30:31], v[28:29]
	s_nop 0
	v_pk_mul_f32 v[30:31], v[24:25], v[28:29]
	v_pk_fma_f32 v[28:29], v[24:25], v[28:29], v[24:25] neg_lo:[1,0,0] neg_hi:[1,0,0]
	s_nop 0
	v_cndmask_b32_e32 v25, v31, v29, vcc
	v_cmp_le_f32_e32 vcc, 0, v24
	s_nop 1
	v_cndmask_b32_e32 v24, v30, v28, vcc
	v_cvt_pk_f16_f32 v24, v24, v25
	v_mul_f32_e64 v25, |v26|, s1
	v_mul_f32_e32 v29, 0xbfb8aa3b, v25
	v_fma_f32 v28, v25, s3, 1.0
	v_mul_f32_e32 v25, v25, v29
	v_exp_f32_e32 v30, v25
	v_mul_f32_e64 v25, |v27|, s1
	v_fma_f32 v29, v25, s3, 1.0
	v_rcp_f32_e32 v28, v28
	v_rcp_f32_e32 v29, v29
	v_mul_f32_e32 v31, 0xbfb8aa3b, v25
	v_mul_f32_e32 v25, v25, v31
	v_exp_f32_e32 v31, v25
	v_pk_fma_f32 v[32:33], v[28:29], s[0:1], v[36:37] op_sel_hi:[1,0,0]
	v_cmp_le_f32_e32 vcc, 0, v27
	v_pk_fma_f32 v[32:33], v[28:29], v[32:33], s[2:3] op_sel_hi:[1,1,0]
	s_nop 0
	v_pk_fma_f32 v[32:33], v[28:29], v[32:33], s[4:5] op_sel_hi:[1,1,0]
	s_nop 0
	v_pk_fma_f32 v[32:33], v[28:29], v[32:33], s[6:7] op_sel_hi:[1,1,0]
	s_nop 0
	v_pk_mul_f32 v[28:29], v[28:29], v[32:33]
	s_nop 0
	v_pk_mul_f32 v[28:29], v[28:29], 0.5 op_sel_hi:[1,0]
	s_nop 0
	v_pk_mul_f32 v[28:29], v[30:31], v[28:29]
	s_nop 0
	v_pk_mul_f32 v[30:31], v[26:27], v[28:29]
	v_pk_fma_f32 v[28:29], v[26:27], v[28:29], v[26:27] neg_lo:[1,0,0] neg_hi:[1,0,0]
	v_mul_f32_e64 v27, |v21|, s1
	v_cndmask_b32_e32 v25, v31, v29, vcc
	v_cmp_le_f32_e32 vcc, 0, v26
	s_nop 1
	v_cndmask_b32_e32 v26, v30, v28, vcc
	v_cvt_pk_f16_f32 v25, v26, v25
	global_store_dwordx2 v[38:39], v[24:25], off offset:192
	v_mul_f32_e64 v25, |v20|, s1
	v_mul_f32_e32 v26, 0xbfb8aa3b, v25
	v_fma_f32 v24, v25, s3, 1.0
	v_mul_f32_e32 v25, v25, v26
	v_exp_f32_e32 v26, v25
	v_fma_f32 v25, v27, s3, 1.0
	v_rcp_f32_e32 v24, v24
	v_rcp_f32_e32 v25, v25
	v_mul_f32_e32 v28, 0xbfb8aa3b, v27
	v_mul_f32_e32 v27, v27, v28
	v_exp_f32_e32 v27, v27
	v_pk_fma_f32 v[28:29], v[24:25], s[0:1], v[36:37] op_sel_hi:[1,0,0]
	v_cmp_le_f32_e32 vcc, 0, v21
	v_pk_fma_f32 v[28:29], v[24:25], v[28:29], s[2:3] op_sel_hi:[1,1,0]
	s_nop 0
	v_pk_fma_f32 v[28:29], v[24:25], v[28:29], s[4:5] op_sel_hi:[1,1,0]
	s_nop 0
	v_pk_fma_f32 v[28:29], v[24:25], v[28:29], s[6:7] op_sel_hi:[1,1,0]
	s_nop 0
	v_pk_mul_f32 v[24:25], v[24:25], v[28:29]
	s_nop 0
	v_pk_mul_f32 v[24:25], v[24:25], 0.5 op_sel_hi:[1,0]
	s_nop 0
	v_pk_mul_f32 v[24:25], v[26:27], v[24:25]
	s_nop 0
	v_pk_mul_f32 v[26:27], v[20:21], v[24:25]
	v_pk_fma_f32 v[24:25], v[20:21], v[24:25], v[20:21] neg_lo:[1,0,0] neg_hi:[1,0,0]
	s_nop 0
	v_cndmask_b32_e32 v21, v27, v25, vcc
	v_cmp_le_f32_e32 vcc, 0, v20
	s_nop 1
	v_cndmask_b32_e32 v20, v26, v24, vcc
	v_cvt_pk_f16_f32 v20, v20, v21
	v_mul_f32_e64 v21, |v22|, s1
	v_mul_f32_e32 v25, 0xbfb8aa3b, v21
	v_fma_f32 v24, v21, s3, 1.0
	v_mul_f32_e32 v21, v21, v25
	v_exp_f32_e32 v26, v21
	v_mul_f32_e64 v21, |v23|, s1
	v_fma_f32 v25, v21, s3, 1.0
	v_rcp_f32_e32 v24, v24
	v_rcp_f32_e32 v25, v25
	v_mul_f32_e32 v27, 0xbfb8aa3b, v21
	v_mul_f32_e32 v21, v21, v27
	v_exp_f32_e32 v27, v21
	v_pk_fma_f32 v[28:29], v[24:25], s[0:1], v[36:37] op_sel_hi:[1,0,0]
	v_cmp_le_f32_e32 vcc, 0, v23
	v_pk_fma_f32 v[28:29], v[24:25], v[28:29], s[2:3] op_sel_hi:[1,1,0]
	s_nop 0
	v_pk_fma_f32 v[28:29], v[24:25], v[28:29], s[4:5] op_sel_hi:[1,1,0]
	s_nop 0
	v_pk_fma_f32 v[28:29], v[24:25], v[28:29], s[6:7] op_sel_hi:[1,1,0]
	s_nop 0
	v_pk_mul_f32 v[24:25], v[24:25], v[28:29]
	s_nop 0
	v_pk_mul_f32 v[24:25], v[24:25], 0.5 op_sel_hi:[1,0]
	s_nop 0
	v_pk_mul_f32 v[24:25], v[26:27], v[24:25]
	s_nop 0
	v_pk_mul_f32 v[26:27], v[22:23], v[24:25]
	v_pk_fma_f32 v[24:25], v[22:23], v[24:25], v[22:23] neg_lo:[1,0,0] neg_hi:[1,0,0]
	v_mul_f32_e64 v23, |v17|, s1
	v_cndmask_b32_e32 v21, v27, v25, vcc
	v_cmp_le_f32_e32 vcc, 0, v22
	s_nop 1
	v_cndmask_b32_e32 v22, v26, v24, vcc
	v_cvt_pk_f16_f32 v21, v22, v21
	global_store_dwordx2 v[38:39], v[20:21], off offset:320
	v_mul_f32_e64 v21, |v16|, s1
	v_mul_f32_e32 v22, 0xbfb8aa3b, v21
	v_fma_f32 v20, v21, s3, 1.0
	v_mul_f32_e32 v21, v21, v22
	v_exp_f32_e32 v22, v21
	v_fma_f32 v21, v23, s3, 1.0
	v_rcp_f32_e32 v20, v20
	v_rcp_f32_e32 v21, v21
	v_mul_f32_e32 v24, 0xbfb8aa3b, v23
	v_mul_f32_e32 v23, v23, v24
	v_exp_f32_e32 v23, v23
	v_pk_fma_f32 v[24:25], v[20:21], s[0:1], v[36:37] op_sel_hi:[1,0,0]
	v_cmp_le_f32_e32 vcc, 0, v17
	v_pk_fma_f32 v[24:25], v[20:21], v[24:25], s[2:3] op_sel_hi:[1,1,0]
	s_nop 0
	v_pk_fma_f32 v[24:25], v[20:21], v[24:25], s[4:5] op_sel_hi:[1,1,0]
	s_nop 0
	v_pk_fma_f32 v[24:25], v[20:21], v[24:25], s[6:7] op_sel_hi:[1,1,0]
	s_nop 0
	v_pk_mul_f32 v[20:21], v[20:21], v[24:25]
	s_nop 0
	v_pk_mul_f32 v[20:21], v[20:21], 0.5 op_sel_hi:[1,0]
	s_nop 0
	v_pk_mul_f32 v[20:21], v[22:23], v[20:21]
	s_nop 0
	v_pk_mul_f32 v[22:23], v[16:17], v[20:21]
	v_pk_fma_f32 v[20:21], v[16:17], v[20:21], v[16:17] neg_lo:[1,0,0] neg_hi:[1,0,0]
	s_nop 0
	v_cndmask_b32_e32 v17, v23, v21, vcc
	v_cmp_le_f32_e32 vcc, 0, v16
	s_nop 1
	v_cndmask_b32_e32 v16, v22, v20, vcc
	v_cvt_pk_f16_f32 v16, v16, v17
	v_mul_f32_e64 v17, |v18|, s1
	v_mul_f32_e32 v21, 0xbfb8aa3b, v17
	v_fma_f32 v20, v17, s3, 1.0
	v_mul_f32_e32 v17, v17, v21
	v_exp_f32_e32 v22, v17
	v_mul_f32_e64 v17, |v19|, s1
	v_fma_f32 v21, v17, s3, 1.0
	v_rcp_f32_e32 v20, v20
	v_rcp_f32_e32 v21, v21
	v_mul_f32_e32 v23, 0xbfb8aa3b, v17
	v_mul_f32_e32 v17, v17, v23
	v_exp_f32_e32 v23, v17
	v_pk_fma_f32 v[24:25], v[20:21], s[0:1], v[36:37] op_sel_hi:[1,0,0]
	v_cmp_le_f32_e32 vcc, 0, v19
	v_pk_fma_f32 v[24:25], v[20:21], v[24:25], s[2:3] op_sel_hi:[1,1,0]
	s_nop 0
	v_pk_fma_f32 v[24:25], v[20:21], v[24:25], s[4:5] op_sel_hi:[1,1,0]
	s_nop 0
	v_pk_fma_f32 v[24:25], v[20:21], v[24:25], s[6:7] op_sel_hi:[1,1,0]
	s_nop 0
	v_pk_mul_f32 v[20:21], v[20:21], v[24:25]
	s_nop 0
	v_pk_mul_f32 v[20:21], v[20:21], 0.5 op_sel_hi:[1,0]
	s_nop 0
	v_pk_mul_f32 v[20:21], v[22:23], v[20:21]
	s_nop 0
	v_pk_mul_f32 v[22:23], v[18:19], v[20:21]
	v_pk_fma_f32 v[20:21], v[18:19], v[20:21], v[18:19] neg_lo:[1,0,0] neg_hi:[1,0,0]
	v_mul_f32_e64 v19, |v13|, s1
	v_cndmask_b32_e32 v17, v23, v21, vcc
	v_cmp_le_f32_e32 vcc, 0, v18
	s_nop 1
	v_cndmask_b32_e32 v18, v22, v20, vcc
	v_cvt_pk_f16_f32 v17, v18, v17
	global_store_dwordx2 v[38:39], v[16:17], off offset:448
	v_mul_f32_e64 v17, |v12|, s1
	v_mul_f32_e32 v18, 0xbfb8aa3b, v17
	v_fma_f32 v16, v17, s3, 1.0
	v_mul_f32_e32 v17, v17, v18
	v_exp_f32_e32 v18, v17
	v_fma_f32 v17, v19, s3, 1.0
	v_rcp_f32_e32 v16, v16
	v_rcp_f32_e32 v17, v17
	v_mul_f32_e32 v20, 0xbfb8aa3b, v19
	v_mul_f32_e32 v19, v19, v20
	v_exp_f32_e32 v19, v19
	v_pk_fma_f32 v[20:21], v[16:17], s[0:1], v[36:37] op_sel_hi:[1,0,0]
	v_cmp_le_f32_e32 vcc, 0, v13
	v_pk_fma_f32 v[20:21], v[16:17], v[20:21], s[2:3] op_sel_hi:[1,1,0]
	s_nop 0
	v_pk_fma_f32 v[20:21], v[16:17], v[20:21], s[4:5] op_sel_hi:[1,1,0]
	s_nop 0
	v_pk_fma_f32 v[20:21], v[16:17], v[20:21], s[6:7] op_sel_hi:[1,1,0]
	s_nop 0
	v_pk_mul_f32 v[16:17], v[16:17], v[20:21]
	s_nop 0
	v_pk_mul_f32 v[16:17], v[16:17], 0.5 op_sel_hi:[1,0]
	s_nop 0
	v_pk_mul_f32 v[16:17], v[18:19], v[16:17]
	s_nop 0
	v_pk_mul_f32 v[18:19], v[12:13], v[16:17]
	v_pk_fma_f32 v[16:17], v[12:13], v[16:17], v[12:13] neg_lo:[1,0,0] neg_hi:[1,0,0]
	s_nop 0
	v_cndmask_b32_e32 v13, v19, v17, vcc
	v_cmp_le_f32_e32 vcc, 0, v12
	s_nop 1
	v_cndmask_b32_e32 v12, v18, v16, vcc
	v_cvt_pk_f16_f32 v12, v12, v13
	v_mul_f32_e64 v13, |v14|, s1
	v_mul_f32_e32 v17, 0xbfb8aa3b, v13
	v_fma_f32 v16, v13, s3, 1.0
	v_mul_f32_e32 v13, v13, v17
	v_exp_f32_e32 v18, v13
	v_mul_f32_e64 v13, |v15|, s1
	v_fma_f32 v17, v13, s3, 1.0
	v_rcp_f32_e32 v16, v16
	v_rcp_f32_e32 v17, v17
	v_mul_f32_e32 v19, 0xbfb8aa3b, v13
	v_mul_f32_e32 v13, v13, v19
	v_exp_f32_e32 v19, v13
	v_pk_fma_f32 v[20:21], v[16:17], s[0:1], v[36:37] op_sel_hi:[1,0,0]
	v_cmp_le_f32_e32 vcc, 0, v15
	v_pk_fma_f32 v[20:21], v[16:17], v[20:21], s[2:3] op_sel_hi:[1,1,0]
	s_nop 0
	v_pk_fma_f32 v[20:21], v[16:17], v[20:21], s[4:5] op_sel_hi:[1,1,0]
	s_nop 0
	v_pk_fma_f32 v[20:21], v[16:17], v[20:21], s[6:7] op_sel_hi:[1,1,0]
	s_nop 0
	v_pk_mul_f32 v[16:17], v[16:17], v[20:21]
	s_nop 0
	v_pk_mul_f32 v[16:17], v[16:17], 0.5 op_sel_hi:[1,0]
	s_nop 0
	v_pk_mul_f32 v[16:17], v[18:19], v[16:17]
	s_nop 0
	v_pk_mul_f32 v[18:19], v[14:15], v[16:17]
	v_pk_fma_f32 v[16:17], v[14:15], v[16:17], v[14:15] neg_lo:[1,0,0] neg_hi:[1,0,0]
	v_mul_f32_e64 v15, |v9|, s1
	v_cndmask_b32_e32 v13, v19, v17, vcc
	v_cmp_le_f32_e32 vcc, 0, v14
	s_nop 1
	v_cndmask_b32_e32 v14, v18, v16, vcc
	v_cvt_pk_f16_f32 v13, v14, v13
	global_store_dwordx2 v[38:39], v[12:13], off offset:96
	v_mul_f32_e64 v13, |v8|, s1
	v_mul_f32_e32 v14, 0xbfb8aa3b, v13
	v_fma_f32 v12, v13, s3, 1.0
	v_mul_f32_e32 v13, v13, v14
	v_exp_f32_e32 v14, v13
	v_fma_f32 v13, v15, s3, 1.0
	v_rcp_f32_e32 v12, v12
	v_rcp_f32_e32 v13, v13
	v_mul_f32_e32 v16, 0xbfb8aa3b, v15
	v_mul_f32_e32 v15, v15, v16
	v_exp_f32_e32 v15, v15
	v_pk_fma_f32 v[16:17], v[12:13], s[0:1], v[36:37] op_sel_hi:[1,0,0]
	v_cmp_le_f32_e32 vcc, 0, v9
	v_pk_fma_f32 v[16:17], v[12:13], v[16:17], s[2:3] op_sel_hi:[1,1,0]
	s_nop 0
	v_pk_fma_f32 v[16:17], v[12:13], v[16:17], s[4:5] op_sel_hi:[1,1,0]
	s_nop 0
	v_pk_fma_f32 v[16:17], v[12:13], v[16:17], s[6:7] op_sel_hi:[1,1,0]
	s_nop 0
	v_pk_mul_f32 v[12:13], v[12:13], v[16:17]
	s_nop 0
	v_pk_mul_f32 v[12:13], v[12:13], 0.5 op_sel_hi:[1,0]
	s_nop 0
	v_pk_mul_f32 v[12:13], v[14:15], v[12:13]
	s_nop 0
	v_pk_mul_f32 v[14:15], v[8:9], v[12:13]
	v_pk_fma_f32 v[12:13], v[8:9], v[12:13], v[8:9] neg_lo:[1,0,0] neg_hi:[1,0,0]
	s_nop 0
	v_cndmask_b32_e32 v9, v15, v13, vcc
	v_cmp_le_f32_e32 vcc, 0, v8
	s_nop 1
	v_cndmask_b32_e32 v8, v14, v12, vcc
	v_cvt_pk_f16_f32 v8, v8, v9
	v_mul_f32_e64 v9, |v10|, s1
	v_mul_f32_e32 v13, 0xbfb8aa3b, v9
	v_fma_f32 v12, v9, s3, 1.0
	v_mul_f32_e32 v9, v9, v13
	v_exp_f32_e32 v14, v9
	v_mul_f32_e64 v9, |v11|, s1
	v_fma_f32 v13, v9, s3, 1.0
	v_rcp_f32_e32 v12, v12
	v_rcp_f32_e32 v13, v13
	v_mul_f32_e32 v15, 0xbfb8aa3b, v9
	v_mul_f32_e32 v9, v9, v15
	v_exp_f32_e32 v15, v9
	v_pk_fma_f32 v[16:17], v[12:13], s[0:1], v[36:37] op_sel_hi:[1,0,0]
	v_cmp_le_f32_e32 vcc, 0, v11
	v_pk_fma_f32 v[16:17], v[12:13], v[16:17], s[2:3] op_sel_hi:[1,1,0]
	s_nop 0
	v_pk_fma_f32 v[16:17], v[12:13], v[16:17], s[4:5] op_sel_hi:[1,1,0]
	s_nop 0
	v_pk_fma_f32 v[16:17], v[12:13], v[16:17], s[6:7] op_sel_hi:[1,1,0]
	s_nop 0
	v_pk_mul_f32 v[12:13], v[12:13], v[16:17]
	s_nop 0
	v_pk_mul_f32 v[12:13], v[12:13], 0.5 op_sel_hi:[1,0]
	s_nop 0
	v_pk_mul_f32 v[12:13], v[14:15], v[12:13]
	s_nop 0
	v_pk_mul_f32 v[14:15], v[10:11], v[12:13]
	v_pk_fma_f32 v[12:13], v[10:11], v[12:13], v[10:11] neg_lo:[1,0,0] neg_hi:[1,0,0]
	v_mul_f32_e64 v11, |v5|, s1
	v_cndmask_b32_e32 v9, v15, v13, vcc
	v_cmp_le_f32_e32 vcc, 0, v10
	s_nop 1
	v_cndmask_b32_e32 v10, v14, v12, vcc
	v_cvt_pk_f16_f32 v9, v10, v9
	global_store_dwordx2 v[38:39], v[8:9], off offset:224
	v_mul_f32_e64 v9, |v4|, s1
	v_mul_f32_e32 v10, 0xbfb8aa3b, v9
	v_fma_f32 v8, v9, s3, 1.0
	v_mul_f32_e32 v9, v9, v10
	v_exp_f32_e32 v10, v9
	v_fma_f32 v9, v11, s3, 1.0
	v_rcp_f32_e32 v8, v8
	v_rcp_f32_e32 v9, v9
	v_mul_f32_e32 v12, 0xbfb8aa3b, v11
	v_mul_f32_e32 v11, v11, v12
	v_exp_f32_e32 v11, v11
	v_pk_fma_f32 v[12:13], v[8:9], s[0:1], v[36:37] op_sel_hi:[1,0,0]
	v_cmp_le_f32_e32 vcc, 0, v5
	v_pk_fma_f32 v[12:13], v[8:9], v[12:13], s[2:3] op_sel_hi:[1,1,0]
	s_nop 0
	v_pk_fma_f32 v[12:13], v[8:9], v[12:13], s[4:5] op_sel_hi:[1,1,0]
	s_nop 0
	v_pk_fma_f32 v[12:13], v[8:9], v[12:13], s[6:7] op_sel_hi:[1,1,0]
	s_nop 0
	v_pk_mul_f32 v[8:9], v[8:9], v[12:13]
	s_nop 0
	v_pk_mul_f32 v[8:9], v[8:9], 0.5 op_sel_hi:[1,0]
	s_nop 0
	v_pk_mul_f32 v[8:9], v[10:11], v[8:9]
	s_nop 0
	v_pk_mul_f32 v[10:11], v[4:5], v[8:9]
	v_pk_fma_f32 v[8:9], v[4:5], v[8:9], v[4:5] neg_lo:[1,0,0] neg_hi:[1,0,0]
	s_nop 0
	v_cndmask_b32_e32 v5, v11, v9, vcc
	v_cmp_le_f32_e32 vcc, 0, v4
	s_nop 1
	v_cndmask_b32_e32 v4, v10, v8, vcc
	v_cvt_pk_f16_f32 v4, v4, v5
	v_mul_f32_e64 v5, |v6|, s1
	v_mul_f32_e32 v9, 0xbfb8aa3b, v5
	v_fma_f32 v8, v5, s3, 1.0
	v_mul_f32_e32 v5, v5, v9
	v_exp_f32_e32 v10, v5
	v_mul_f32_e64 v5, |v7|, s1
	v_fma_f32 v9, v5, s3, 1.0
	v_rcp_f32_e32 v8, v8
	v_rcp_f32_e32 v9, v9
	v_mul_f32_e32 v11, 0xbfb8aa3b, v5
	v_mul_f32_e32 v5, v5, v11
	v_exp_f32_e32 v11, v5
	v_pk_fma_f32 v[12:13], v[8:9], s[0:1], v[36:37] op_sel_hi:[1,0,0]
	v_cmp_le_f32_e32 vcc, 0, v7
	v_pk_fma_f32 v[12:13], v[8:9], v[12:13], s[2:3] op_sel_hi:[1,1,0]
	s_nop 0
	v_pk_fma_f32 v[12:13], v[8:9], v[12:13], s[4:5] op_sel_hi:[1,1,0]
	s_nop 0
	v_pk_fma_f32 v[12:13], v[8:9], v[12:13], s[6:7] op_sel_hi:[1,1,0]
	s_nop 0
	v_pk_mul_f32 v[8:9], v[8:9], v[12:13]
	s_nop 0
	v_pk_mul_f32 v[8:9], v[8:9], 0.5 op_sel_hi:[1,0]
	s_nop 0
	v_pk_mul_f32 v[8:9], v[10:11], v[8:9]
	s_nop 0
	v_pk_mul_f32 v[10:11], v[6:7], v[8:9]
	v_pk_fma_f32 v[8:9], v[6:7], v[8:9], v[6:7] neg_lo:[1,0,0] neg_hi:[1,0,0]
	v_mul_f32_e64 v7, |v1|, s1
	v_cndmask_b32_e32 v5, v11, v9, vcc
	v_cmp_le_f32_e32 vcc, 0, v6
	s_nop 1
	v_cndmask_b32_e32 v6, v10, v8, vcc
	v_cvt_pk_f16_f32 v5, v6, v5
	global_store_dwordx2 v[38:39], v[4:5], off offset:352
	v_mul_f32_e64 v5, |v0|, s1
	v_mul_f32_e32 v6, 0xbfb8aa3b, v5
	v_fma_f32 v4, v5, s3, 1.0
	v_mul_f32_e32 v5, v5, v6
	v_exp_f32_e32 v6, v5
	v_fma_f32 v5, v7, s3, 1.0
	v_rcp_f32_e32 v4, v4
	v_rcp_f32_e32 v5, v5
	v_mul_f32_e32 v8, 0xbfb8aa3b, v7
	v_mul_f32_e32 v7, v7, v8
	v_exp_f32_e32 v7, v7
	v_pk_fma_f32 v[8:9], v[4:5], s[0:1], v[36:37] op_sel_hi:[1,0,0]
	v_cmp_le_f32_e32 vcc, 0, v1
	v_pk_fma_f32 v[8:9], v[4:5], v[8:9], s[2:3] op_sel_hi:[1,1,0]
	s_nop 0
	v_pk_fma_f32 v[8:9], v[4:5], v[8:9], s[4:5] op_sel_hi:[1,1,0]
	s_nop 0
	v_pk_fma_f32 v[8:9], v[4:5], v[8:9], s[6:7] op_sel_hi:[1,1,0]
	s_nop 0
	v_pk_mul_f32 v[4:5], v[4:5], v[8:9]
	s_nop 0
	v_pk_mul_f32 v[4:5], v[4:5], 0.5 op_sel_hi:[1,0]
	s_nop 0
	v_pk_mul_f32 v[4:5], v[6:7], v[4:5]
	s_nop 0
	v_pk_mul_f32 v[6:7], v[0:1], v[4:5]
	v_pk_fma_f32 v[4:5], v[0:1], v[4:5], v[0:1] neg_lo:[1,0,0] neg_hi:[1,0,0]
	s_nop 0
	v_cndmask_b32_e32 v1, v7, v5, vcc
	v_cmp_le_f32_e32 vcc, 0, v0
	s_nop 1
	v_cndmask_b32_e32 v0, v6, v4, vcc
	v_cvt_pk_f16_f32 v0, v0, v1
	v_mul_f32_e64 v1, |v2|, s1
	v_mul_f32_e32 v5, 0xbfb8aa3b, v1
	v_fma_f32 v4, v1, s3, 1.0
	v_mul_f32_e32 v1, v1, v5
	v_exp_f32_e32 v6, v1
	v_mul_f32_e64 v1, |v3|, s1
	v_fma_f32 v5, v1, s3, 1.0
	v_rcp_f32_e32 v4, v4
	v_rcp_f32_e32 v5, v5
	v_mul_f32_e32 v7, 0xbfb8aa3b, v1
	v_mul_f32_e32 v1, v1, v7
	v_exp_f32_e32 v7, v1
	v_pk_fma_f32 v[8:9], v[4:5], s[0:1], v[36:37] op_sel_hi:[1,0,0]
	v_cmp_le_f32_e32 vcc, 0, v3
	v_pk_fma_f32 v[8:9], v[4:5], v[8:9], s[2:3] op_sel_hi:[1,1,0]
	s_nop 0
	v_pk_fma_f32 v[8:9], v[4:5], v[8:9], s[4:5] op_sel_hi:[1,1,0]
	s_nop 0
	v_pk_fma_f32 v[8:9], v[4:5], v[8:9], s[6:7] op_sel_hi:[1,1,0]
	s_nop 0
	v_pk_mul_f32 v[4:5], v[4:5], v[8:9]
	s_nop 0
	v_pk_mul_f32 v[4:5], v[4:5], 0.5 op_sel_hi:[1,0]
	s_nop 0
	v_pk_mul_f32 v[4:5], v[6:7], v[4:5]
	s_nop 0
	v_pk_mul_f32 v[6:7], v[2:3], v[4:5]
	v_pk_fma_f32 v[4:5], v[2:3], v[4:5], v[2:3] neg_lo:[1,0,0] neg_hi:[1,0,0]
	s_nop 0
	v_cndmask_b32_e32 v1, v7, v5, vcc
	v_cmp_le_f32_e32 vcc, 0, v2
	s_nop 1
	v_cndmask_b32_e32 v2, v6, v4, vcc
	v_cvt_pk_f16_f32 v1, v2, v1
	global_store_dwordx2 v[38:39], v[0:1], off offset:480
	s_endpgm
